# FFT phase: B-fragment LDS reads of the sixteen 16-MFMA chains run three fragments ahead in rotating registers with counted waits
# speedup vs baseline: 1.0142x; 1.0006x over previous
; __device__ __forceinline__ unsigned cvt2_bf16(float lo, float hi) { unsigned r; asm("v_cvt_pk_bf16_f32 %0, %1, %2" : "=v"(r) : "v"(lo), "v"(hi)); return r; }
; __device__ __forceinline__ int crow(int r, int hi) { return (r & 3) + 8 * (r >> 2) + 4 * hi; }
; __device__ __forceinline__ int crow(int r, int hi) { return (r & 3) + 8 * (r >> 2) + 4 * hi; }
; __device__ __forceinline__ int crow(int r, int hi) { return (r & 3) + 8 * (r >> 2) + 4 * hi; }
;     __device__ __forceinline__ const float* c() const { return (const float*)ld(1); }
;     __device__ __forceinline__ float* out() const { return (float*)ld(25); }
; __device__ __forceinline__ void fft_phase_split(const bf16_t* __restrict__ WCT, bf16_t* __restrict__ FB, const bf16_t* __restrict__ A1T, const bf16_t* __restrict__ A2T, const float* __restrict__ TW, char* lds, int G) {
;     ...
;       for (int c = 0; c < 8; ++c) {
;           const bf16_t* Zs = (const bf16_t*)(lds + ((c & 1) ? R_Z1 : R_Z0));
; #pragma unroll
;           for (int nbp = 0; nbp < 2; ++nbp) { const int k1o = 32 * nbp + r32; f32x16 out = f32x16{};
; #pragma unroll
;             for (int ks = 0; ks < 16; ++ks) { const bf16x8 bfr = *(const bf16x8*)(Zs + ((ks >> 3) * 64 + k1o) * ZST + (ks & 7) * 16 + 8 * hi);
;               out = __builtin_amdgcn_mfma_f32_32x32x16_bf16(a2[ks], bfr, out, 0, 0, 0); }
; #pragma unroll
;             for (int r = 0; r < 16; ++r) { const unsigned w = cvt2_bf16(out[r] * SC, out[r] * SC);
;               if ((c & 1) == 0) o[nbp][r][c >> 1] = w & 0xffffu; else o[nbp][r][c >> 1] |= w & 0xffff0000u; } }
;           if (c == 7) {
; #pragma unroll
;             for (int nbp = 0; nbp < 2; ++nbp)
; #pragma unroll
;               for (int r = 0; r < 16; ++r) { const int k = 32 * nbp + r32 + 64 * (32 * mb + crow(r, hi)); *(u32x4*)(fb + (size_t)k * 8) = o[nbp][r]; } }
;           __syncthreads();
.LBB0_1547:
	s_barrier
	s_barrier
	ds_read_b128 v[244:247], v224
	ds_read_b128 v[250:253], v224 offset:32
	ds_read_b128 v[82:85], v224 offset:64
	s_waitcnt lgkmcnt(2)
	v_mfma_f32_32x32x16_bf16 v[2:17], v[74:77], v[244:247], 0
	v_add_u32_e32 v97, v220, v219
	v_add_u32_e32 v93, v220, v221
	v_add_u32_e32 v153, v223, v221
	s_add_i32 s5, s5, s8
	s_cmpk_lt_i32 s5, 0x100
	ds_read_b128 v[244:247], v224 offset:96
	s_waitcnt lgkmcnt(2)
	v_mfma_f32_32x32x16_bf16 v[2:17], v[18:21], v[250:253], v[2:17]
	ds_read_b128 v[250:253], v224 offset:128
	s_waitcnt lgkmcnt(2)
	v_mfma_f32_32x32x16_bf16 v[2:17], v[22:25], v[82:85], v[2:17]
	ds_read_b128 v[82:85], v224 offset:160
	s_waitcnt lgkmcnt(2)
	v_mfma_f32_32x32x16_bf16 v[2:17], v[26:29], v[244:247], v[2:17]
	ds_read_b128 v[244:247], v224 offset:192
	s_waitcnt lgkmcnt(2)
	v_mfma_f32_32x32x16_bf16 v[2:17], v[30:33], v[250:253], v[2:17]
	ds_read_b128 v[250:253], v224 offset:224
	s_waitcnt lgkmcnt(2)
	v_mfma_f32_32x32x16_bf16 v[2:17], v[34:37], v[82:85], v[2:17]
	ds_read_b128 v[82:85], v97
	s_waitcnt lgkmcnt(2)
	v_mfma_f32_32x32x16_bf16 v[2:17], v[38:41], v[244:247], v[2:17]
	ds_read_b128 v[244:247], v225 offset:32
	s_waitcnt lgkmcnt(2)
	v_mfma_f32_32x32x16_bf16 v[2:17], v[42:45], v[250:253], v[2:17]
	ds_read_b128 v[250:253], v225 offset:64
	s_waitcnt lgkmcnt(2)
	v_mfma_f32_32x32x16_bf16 v[2:17], v[46:49], v[82:85], v[2:17]
	ds_read_b128 v[82:85], v225 offset:96
	s_waitcnt lgkmcnt(2)
	v_mfma_f32_32x32x16_bf16 v[2:17], v[50:53], v[244:247], v[2:17]
	ds_read_b128 v[244:247], v225 offset:128
	s_waitcnt lgkmcnt(2)
	v_mfma_f32_32x32x16_bf16 v[2:17], v[54:57], v[250:253], v[2:17]
	ds_read_b128 v[250:253], v225 offset:160
	s_waitcnt lgkmcnt(2)
	v_mfma_f32_32x32x16_bf16 v[2:17], v[58:61], v[82:85], v[2:17]
	ds_read_b128 v[82:85], v225 offset:192
	s_waitcnt lgkmcnt(2)
	v_mfma_f32_32x32x16_bf16 v[2:17], v[62:65], v[244:247], v[2:17]
	ds_read_b128 v[244:247], v225 offset:224
	s_waitcnt lgkmcnt(2)
	v_mfma_f32_32x32x16_bf16 v[2:17], v[66:69], v[250:253], v[2:17]
	s_waitcnt lgkmcnt(1)
	v_mfma_f32_32x32x16_bf16 v[2:17], v[70:73], v[82:85], v[2:17]
	s_waitcnt lgkmcnt(0)
	v_mfma_f32_32x32x16_bf16 v[2:17], v[78:81], v[244:247], v[2:17]
	s_nop 11
	v_mul_f32_e32 v2, 0x3a000000, v2
	v_cvt_pk_bf16_f32 v90, v2, v2
	v_mul_f32_e32 v2, 0x3a000000, v3
	v_cvt_pk_bf16_f32 v94, v2, v2
	v_mul_f32_e32 v2, 0x3a000000, v4
	v_cvt_pk_bf16_f32 v102, v2, v2
	v_mul_f32_e32 v2, 0x3a000000, v5
	v_cvt_pk_bf16_f32 v106, v2, v2
	v_mul_f32_e32 v2, 0x3a000000, v6
	v_cvt_pk_bf16_f32 v109, v2, v2
	v_mul_f32_e32 v2, 0x3a000000, v7
	v_cvt_pk_bf16_f32 v118, v2, v2
	v_mul_f32_e32 v2, 0x3a000000, v8
	v_cvt_pk_bf16_f32 v119, v2, v2
	v_mul_f32_e32 v2, 0x3a000000, v9
	v_cvt_pk_bf16_f32 v120, v2, v2
	v_mul_f32_e32 v2, 0x3a000000, v10
	v_cvt_pk_bf16_f32 v121, v2, v2
	v_mul_f32_e32 v2, 0x3a000000, v11
	v_cvt_pk_bf16_f32 v123, v2, v2
	v_mul_f32_e32 v2, 0x3a000000, v12
	v_cvt_pk_bf16_f32 v124, v2, v2
	v_mul_f32_e32 v2, 0x3a000000, v13
	v_cvt_pk_bf16_f32 v125, v2, v2
	v_mul_f32_e32 v2, 0x3a000000, v14
	v_cvt_pk_bf16_f32 v127, v2, v2
	v_mul_f32_e32 v2, 0x3a000000, v15
	v_cvt_pk_bf16_f32 v128, v2, v2
	v_mul_f32_e32 v2, 0x3a000000, v16
	v_cvt_pk_bf16_f32 v129, v2, v2
	v_mul_f32_e32 v2, 0x3a000000, v17
	v_cvt_pk_bf16_f32 v131, v2, v2
	ds_read_b128 v[244:247], v93
	ds_read_b128 v[250:253], v226 offset:32
	ds_read_b128 v[82:85], v226 offset:64
	s_waitcnt lgkmcnt(2)
	v_mfma_f32_32x32x16_bf16 v[2:17], v[74:77], v[244:247], 0
	ds_read_b128 v[244:247], v226 offset:96
	s_waitcnt lgkmcnt(2)
	v_mfma_f32_32x32x16_bf16 v[2:17], v[18:21], v[250:253], v[2:17]
	ds_read_b128 v[250:253], v226 offset:128
	s_waitcnt lgkmcnt(2)
	v_mfma_f32_32x32x16_bf16 v[2:17], v[22:25], v[82:85], v[2:17]
	v_add_u32_e32 v89, v220, v222
	ds_read_b128 v[82:85], v226 offset:160
	s_waitcnt lgkmcnt(2)
	v_mfma_f32_32x32x16_bf16 v[2:17], v[26:29], v[244:247], v[2:17]
	ds_read_b128 v[244:247], v226 offset:192
	s_waitcnt lgkmcnt(2)
	v_mfma_f32_32x32x16_bf16 v[2:17], v[30:33], v[250:253], v[2:17]
	ds_read_b128 v[250:253], v226 offset:224
	s_waitcnt lgkmcnt(2)
	v_mfma_f32_32x32x16_bf16 v[2:17], v[34:37], v[82:85], v[2:17]
	ds_read_b128 v[82:85], v89
	s_waitcnt lgkmcnt(2)
	v_mfma_f32_32x32x16_bf16 v[2:17], v[38:41], v[244:247], v[2:17]
	ds_read_b128 v[244:247], v227 offset:32
	s_waitcnt lgkmcnt(2)
	v_mfma_f32_32x32x16_bf16 v[2:17], v[42:45], v[250:253], v[2:17]
	ds_read_b128 v[250:253], v227 offset:64
	s_waitcnt lgkmcnt(2)
	v_mfma_f32_32x32x16_bf16 v[2:17], v[46:49], v[82:85], v[2:17]
	ds_read_b128 v[82:85], v227 offset:96
	s_waitcnt lgkmcnt(2)
	v_mfma_f32_32x32x16_bf16 v[2:17], v[50:53], v[244:247], v[2:17]
	ds_read_b128 v[244:247], v227 offset:128
	s_waitcnt lgkmcnt(2)
	v_mfma_f32_32x32x16_bf16 v[2:17], v[54:57], v[250:253], v[2:17]
	ds_read_b128 v[250:253], v227 offset:160
	s_waitcnt lgkmcnt(2)
	v_mfma_f32_32x32x16_bf16 v[2:17], v[58:61], v[82:85], v[2:17]
	ds_read_b128 v[82:85], v227 offset:192
	s_waitcnt lgkmcnt(2)
	v_mfma_f32_32x32x16_bf16 v[2:17], v[62:65], v[244:247], v[2:17]
	ds_read_b128 v[244:247], v227 offset:224
	s_waitcnt lgkmcnt(2)
	v_mfma_f32_32x32x16_bf16 v[2:17], v[66:69], v[250:253], v[2:17]
	s_waitcnt lgkmcnt(1)
	v_mfma_f32_32x32x16_bf16 v[2:17], v[70:73], v[82:85], v[2:17]
	s_waitcnt lgkmcnt(0)
	s_barrier
; __device__ __forceinline__ unsigned cvt2_bf16(float lo, float hi) { unsigned r; asm("v_cvt_pk_bf16_f32 %0, %1, %2" : "=v"(r) : "v"(lo), "v"(hi)); return r; }
; __device__ __forceinline__ int crow(int r, int hi) { return (r & 3) + 8 * (r >> 2) + 4 * hi; }
; __device__ __forceinline__ int crow(int r, int hi) { return (r & 3) + 8 * (r >> 2) + 4 * hi; }
; __device__ __forceinline__ int crow(int r, int hi) { return (r & 3) + 8 * (r >> 2) + 4 * hi; }
;     __device__ __forceinline__ const float* c() const { return (const float*)ld(1); }
;     __device__ __forceinline__ float* out() const { return (float*)ld(25); }
; __device__ __forceinline__ void fft_phase_split(const bf16_t* __restrict__ WCT, bf16_t* __restrict__ FB, const bf16_t* __restrict__ A1T, const bf16_t* __restrict__ A2T, const float* __restrict__ TW, char* lds, int G) {
;     ...
;       for (int c = 0; c < 8; ++c) {
;           const bf16_t* Zs = (const bf16_t*)(lds + ((c & 1) ? R_Z1 : R_Z0));
; #pragma unroll
;           for (int nbp = 0; nbp < 2; ++nbp) { const int k1o = 32 * nbp + r32; f32x16 out = f32x16{};
; #pragma unroll
;             for (int ks = 0; ks < 16; ++ks) { const bf16x8 bfr = *(const bf16x8*)(Zs + ((ks >> 3) * 64 + k1o) * ZST + (ks & 7) * 16 + 8 * hi);
;               out = __builtin_amdgcn_mfma_f32_32x32x16_bf16(a2[ks], bfr, out, 0, 0, 0); }
; #pragma unroll
;             for (int r = 0; r < 16; ++r) { const unsigned w = cvt2_bf16(out[r] * SC, out[r] * SC);
;               if ((c & 1) == 0) o[nbp][r][c >> 1] = w & 0xffffu; else o[nbp][r][c >> 1] |= w & 0xffff0000u; } }
;           if (c == 7) {
; #pragma unroll
;             for (int nbp = 0; nbp < 2; ++nbp)
; #pragma unroll
;               for (int r = 0; r < 16; ++r) { const int k = 32 * nbp + r32 + 64 * (32 * mb + crow(r, hi)); *(u32x4*)(fb + (size_t)k * 8) = o[nbp][r]; } }
;           __syncthreads();
	v_mfma_f32_32x32x16_bf16 v[2:17], v[78:81], v[244:247], v[2:17]
	v_add_u32_e32 v85, v223, v219
	s_nop 10
	v_mul_f32_e32 v2, 0x3a000000, v2
	v_cvt_pk_bf16_f32 v108, v2, v2
	v_mul_f32_e32 v2, 0x3a000000, v3
	v_cvt_pk_bf16_f32 v107, v2, v2
	v_mul_f32_e32 v2, 0x3a000000, v4
	v_cvt_pk_bf16_f32 v105, v2, v2
	v_mul_f32_e32 v2, 0x3a000000, v5
	v_cvt_pk_bf16_f32 v104, v2, v2
	v_mul_f32_e32 v2, 0x3a000000, v6
	v_cvt_pk_bf16_f32 v103, v2, v2
	v_mul_f32_e32 v2, 0x3a000000, v7
	v_cvt_pk_bf16_f32 v101, v2, v2
	v_mul_f32_e32 v2, 0x3a000000, v8
	v_cvt_pk_bf16_f32 v100, v2, v2
	v_mul_f32_e32 v2, 0x3a000000, v9
	v_cvt_pk_bf16_f32 v99, v2, v2
	v_mul_f32_e32 v2, 0x3a000000, v10
	v_cvt_pk_bf16_f32 v96, v2, v2
	v_mul_f32_e32 v2, 0x3a000000, v11
	v_cvt_pk_bf16_f32 v95, v2, v2
	v_mul_f32_e32 v2, 0x3a000000, v12
	v_cvt_pk_bf16_f32 v92, v2, v2
	v_mul_f32_e32 v2, 0x3a000000, v13
	v_cvt_pk_bf16_f32 v91, v2, v2
	v_mul_f32_e32 v2, 0x3a000000, v14
	v_cvt_pk_bf16_f32 v88, v2, v2
	v_mul_f32_e32 v2, 0x3a000000, v15
	v_cvt_pk_bf16_f32 v87, v2, v2
	v_mul_f32_e32 v2, 0x3a000000, v16
	v_cvt_pk_bf16_f32 v84, v2, v2
	v_mul_f32_e32 v2, 0x3a000000, v17
	v_cvt_pk_bf16_f32 v83, v2, v2
	ds_read_b128 v[244:247], v228
	ds_read_b128 v[250:253], v228 offset:32
	ds_read_b128 v[110:113], v228 offset:64
	s_waitcnt lgkmcnt(2)
	v_mfma_f32_32x32x16_bf16 v[2:17], v[74:77], v[244:247], 0
	ds_read_b128 v[244:247], v228 offset:96
	s_waitcnt lgkmcnt(2)
	v_mfma_f32_32x32x16_bf16 v[2:17], v[18:21], v[250:253], v[2:17]
	ds_read_b128 v[250:253], v228 offset:128
	s_waitcnt lgkmcnt(2)
	v_mfma_f32_32x32x16_bf16 v[2:17], v[22:25], v[110:113], v[2:17]
	ds_read_b128 v[110:113], v228 offset:160
	s_waitcnt lgkmcnt(2)
	v_mfma_f32_32x32x16_bf16 v[2:17], v[26:29], v[244:247], v[2:17]
	ds_read_b128 v[244:247], v228 offset:192
	s_waitcnt lgkmcnt(2)
	v_mfma_f32_32x32x16_bf16 v[2:17], v[30:33], v[250:253], v[2:17]
	ds_read_b128 v[250:253], v228 offset:224
	s_waitcnt lgkmcnt(2)
	v_mfma_f32_32x32x16_bf16 v[2:17], v[34:37], v[110:113], v[2:17]
	ds_read_b128 v[110:113], v85
	s_waitcnt lgkmcnt(2)
	v_mfma_f32_32x32x16_bf16 v[2:17], v[38:41], v[244:247], v[2:17]
	ds_read_b128 v[244:247], v229 offset:32
	s_waitcnt lgkmcnt(2)
	v_mfma_f32_32x32x16_bf16 v[2:17], v[42:45], v[250:253], v[2:17]
	ds_read_b128 v[250:253], v229 offset:64
	s_waitcnt lgkmcnt(2)
	v_mfma_f32_32x32x16_bf16 v[2:17], v[46:49], v[110:113], v[2:17]
	ds_read_b128 v[110:113], v229 offset:96
	s_waitcnt lgkmcnt(2)
	v_mfma_f32_32x32x16_bf16 v[2:17], v[50:53], v[244:247], v[2:17]
	ds_read_b128 v[244:247], v229 offset:128
	s_waitcnt lgkmcnt(2)
	v_mfma_f32_32x32x16_bf16 v[2:17], v[54:57], v[250:253], v[2:17]
	ds_read_b128 v[250:253], v229 offset:160
	s_waitcnt lgkmcnt(2)
	v_mfma_f32_32x32x16_bf16 v[2:17], v[58:61], v[110:113], v[2:17]
	ds_read_b128 v[110:113], v229 offset:192
	s_waitcnt lgkmcnt(2)
	v_mfma_f32_32x32x16_bf16 v[2:17], v[62:65], v[244:247], v[2:17]
	ds_read_b128 v[244:247], v229 offset:224
	s_waitcnt lgkmcnt(2)
	v_mfma_f32_32x32x16_bf16 v[2:17], v[66:69], v[250:253], v[2:17]
	s_waitcnt lgkmcnt(1)
	v_mfma_f32_32x32x16_bf16 v[2:17], v[70:73], v[110:113], v[2:17]
	s_waitcnt lgkmcnt(0)
	v_mfma_f32_32x32x16_bf16 v[2:17], v[78:81], v[244:247], v[2:17]
	s_nop 11
	v_mul_f32_e32 v2, 0x3a000000, v2
	v_cvt_pk_bf16_f32 v2, v2, v2
	s_nop 0
	v_bfi_b32 v130, s0, v2, v90
	v_mul_f32_e32 v2, 0x3a000000, v3
	v_cvt_pk_bf16_f32 v2, v2, v2
	s_nop 0
	v_bfi_b32 v134, s0, v2, v94
	v_mul_f32_e32 v2, 0x3a000000, v4
	v_cvt_pk_bf16_f32 v2, v2, v2
	s_nop 0
	v_bfi_b32 v138, s0, v2, v102
	v_mul_f32_e32 v2, 0x3a000000, v5
	v_cvt_pk_bf16_f32 v2, v2, v2
	s_nop 0
	v_bfi_b32 v142, s0, v2, v106
	v_mul_f32_e32 v2, 0x3a000000, v6
	v_cvt_pk_bf16_f32 v2, v2, v2
	s_nop 0
	v_bfi_b32 v114, s0, v2, v109
	v_mul_f32_e32 v2, 0x3a000000, v7
	v_cvt_pk_bf16_f32 v2, v2, v2
	s_nop 0
	v_bfi_b32 v118, s0, v2, v118
	v_mul_f32_e32 v2, 0x3a000000, v8
	v_cvt_pk_bf16_f32 v2, v2, v2
	s_nop 0
	v_bfi_b32 v122, s0, v2, v119
	v_mul_f32_e32 v2, 0x3a000000, v9
	v_cvt_pk_bf16_f32 v2, v2, v2
	s_nop 0
	v_bfi_b32 v126, s0, v2, v120
	v_mul_f32_e32 v2, 0x3a000000, v10
	v_cvt_pk_bf16_f32 v2, v2, v2
	s_nop 0
	v_bfi_b32 v82, s0, v2, v121
	v_mul_f32_e32 v2, 0x3a000000, v11
	v_cvt_pk_bf16_f32 v2, v2, v2
	s_nop 0
	v_bfi_b32 v86, s0, v2, v123
	v_mul_f32_e32 v2, 0x3a000000, v12
	v_cvt_pk_bf16_f32 v2, v2, v2
	s_nop 0
	v_bfi_b32 v90, s0, v2, v124
	v_mul_f32_e32 v2, 0x3a000000, v13
	v_cvt_pk_bf16_f32 v2, v2, v2
	s_nop 0
	v_bfi_b32 v94, s0, v2, v125
	v_mul_f32_e32 v2, 0x3a000000, v14
	v_cvt_pk_bf16_f32 v2, v2, v2
	s_nop 0
	v_bfi_b32 v98, s0, v2, v127
	v_mul_f32_e32 v2, 0x3a000000, v15
	v_cvt_pk_bf16_f32 v2, v2, v2
	s_nop 0
	v_bfi_b32 v102, s0, v2, v128
	v_mul_f32_e32 v2, 0x3a000000, v16
	v_cvt_pk_bf16_f32 v2, v2, v2
	s_nop 0
	v_bfi_b32 v106, s0, v2, v129
	v_mul_f32_e32 v2, 0x3a000000, v17
	v_cvt_pk_bf16_f32 v2, v2, v2
	s_nop 0
	v_bfi_b32 v110, s0, v2, v131
	ds_read_b128 v[244:247], v153
	ds_read_b128 v[250:253], v230 offset:32
	ds_read_b128 v[144:147], v230 offset:64
	s_waitcnt lgkmcnt(2)
	v_mfma_f32_32x32x16_bf16 v[2:17], v[74:77], v[244:247], 0
	ds_read_b128 v[244:247], v230 offset:96
	s_waitcnt lgkmcnt(2)
	v_mfma_f32_32x32x16_bf16 v[2:17], v[18:21], v[250:253], v[2:17]
	ds_read_b128 v[250:253], v230 offset:128
	s_waitcnt lgkmcnt(2)
	v_mfma_f32_32x32x16_bf16 v[2:17], v[22:25], v[144:147], v[2:17]
	v_add_u32_e32 v149, v223, v222
	ds_read_b128 v[144:147], v230 offset:160
	s_waitcnt lgkmcnt(2)
	v_mfma_f32_32x32x16_bf16 v[2:17], v[26:29], v[244:247], v[2:17]
	ds_read_b128 v[244:247], v230 offset:192
	s_waitcnt lgkmcnt(2)
	v_mfma_f32_32x32x16_bf16 v[2:17], v[30:33], v[250:253], v[2:17]
	ds_read_b128 v[250:253], v230 offset:224
	s_waitcnt lgkmcnt(2)
	v_mfma_f32_32x32x16_bf16 v[2:17], v[34:37], v[144:147], v[2:17]
	ds_read_b128 v[144:147], v149
	s_waitcnt lgkmcnt(2)
	v_mfma_f32_32x32x16_bf16 v[2:17], v[38:41], v[244:247], v[2:17]
	ds_read_b128 v[244:247], v231 offset:32
	s_waitcnt lgkmcnt(2)
	v_mfma_f32_32x32x16_bf16 v[2:17], v[42:45], v[250:253], v[2:17]
	ds_read_b128 v[250:253], v231 offset:64
	s_waitcnt lgkmcnt(2)
	v_mfma_f32_32x32x16_bf16 v[2:17], v[46:49], v[144:147], v[2:17]
	ds_read_b128 v[144:147], v231 offset:96
	s_waitcnt lgkmcnt(2)
	v_mfma_f32_32x32x16_bf16 v[2:17], v[50:53], v[244:247], v[2:17]
	ds_read_b128 v[244:247], v231 offset:128
	s_waitcnt lgkmcnt(2)
	v_mfma_f32_32x32x16_bf16 v[2:17], v[54:57], v[250:253], v[2:17]
	ds_read_b128 v[250:253], v231 offset:160
	s_waitcnt lgkmcnt(2)
	v_mfma_f32_32x32x16_bf16 v[2:17], v[58:61], v[144:147], v[2:17]
	ds_read_b128 v[144:147], v231 offset:192
	s_waitcnt lgkmcnt(2)
	v_mfma_f32_32x32x16_bf16 v[2:17], v[62:65], v[244:247], v[2:17]
	ds_read_b128 v[244:247], v231 offset:224
	s_waitcnt lgkmcnt(2)
	v_mfma_f32_32x32x16_bf16 v[2:17], v[66:69], v[250:253], v[2:17]
	s_waitcnt lgkmcnt(1)
	v_mfma_f32_32x32x16_bf16 v[2:17], v[70:73], v[144:147], v[2:17]
	s_waitcnt lgkmcnt(0)
	s_barrier
; __device__ __forceinline__ unsigned cvt2_bf16(float lo, float hi) { unsigned r; asm("v_cvt_pk_bf16_f32 %0, %1, %2" : "=v"(r) : "v"(lo), "v"(hi)); return r; }
; __device__ __forceinline__ int crow(int r, int hi) { return (r & 3) + 8 * (r >> 2) + 4 * hi; }
; __device__ __forceinline__ int crow(int r, int hi) { return (r & 3) + 8 * (r >> 2) + 4 * hi; }
; __device__ __forceinline__ int crow(int r, int hi) { return (r & 3) + 8 * (r >> 2) + 4 * hi; }
;     __device__ __forceinline__ const float* c() const { return (const float*)ld(1); }
;     __device__ __forceinline__ float* out() const { return (float*)ld(25); }
; __device__ __forceinline__ void fft_phase_split(const bf16_t* __restrict__ WCT, bf16_t* __restrict__ FB, const bf16_t* __restrict__ A1T, const bf16_t* __restrict__ A2T, const float* __restrict__ TW, char* lds, int G) {
;     ...
;       for (int c = 0; c < 8; ++c) {
;           const bf16_t* Zs = (const bf16_t*)(lds + ((c & 1) ? R_Z1 : R_Z0));
; #pragma unroll
;           for (int nbp = 0; nbp < 2; ++nbp) { const int k1o = 32 * nbp + r32; f32x16 out = f32x16{};
; #pragma unroll
;             for (int ks = 0; ks < 16; ++ks) { const bf16x8 bfr = *(const bf16x8*)(Zs + ((ks >> 3) * 64 + k1o) * ZST + (ks & 7) * 16 + 8 * hi);
;               out = __builtin_amdgcn_mfma_f32_32x32x16_bf16(a2[ks], bfr, out, 0, 0, 0); }
; #pragma unroll
;             for (int r = 0; r < 16; ++r) { const unsigned w = cvt2_bf16(out[r] * SC, out[r] * SC);
;               if ((c & 1) == 0) o[nbp][r][c >> 1] = w & 0xffffu; else o[nbp][r][c >> 1] |= w & 0xffff0000u; } }
;           if (c == 7) {
; #pragma unroll
;             for (int nbp = 0; nbp < 2; ++nbp)
; #pragma unroll
;               for (int r = 0; r < 16; ++r) { const int k = 32 * nbp + r32 + 64 * (32 * mb + crow(r, hi)); *(u32x4*)(fb + (size_t)k * 8) = o[nbp][r]; } }
;           __syncthreads();
	v_mfma_f32_32x32x16_bf16 v[2:17], v[78:81], v[244:247], v[2:17]
	s_nop 11
	v_mul_f32_e32 v2, 0x3a000000, v2
	v_cvt_pk_bf16_f32 v2, v2, v2
	s_nop 0
	v_bfi_b32 v146, s0, v2, v108
	v_mul_f32_e32 v2, 0x3a000000, v3
	v_cvt_pk_bf16_f32 v2, v2, v2
	s_nop 0
	v_bfi_b32 v150, s0, v2, v107
	v_mul_f32_e32 v2, 0x3a000000, v4
	v_cvt_pk_bf16_f32 v2, v2, v2
	s_nop 0
	v_bfi_b32 v154, s0, v2, v105
	v_mul_f32_e32 v2, 0x3a000000, v5
	v_cvt_pk_bf16_f32 v2, v2, v2
	s_nop 0
	v_bfi_b32 v158, s0, v2, v104
	v_mul_f32_e32 v2, 0x3a000000, v6
	v_cvt_pk_bf16_f32 v2, v2, v2
	s_nop 0
	v_bfi_b32 v162, s0, v2, v103
	v_mul_f32_e32 v2, 0x3a000000, v7
	v_cvt_pk_bf16_f32 v2, v2, v2
	s_nop 0
	v_bfi_b32 v166, s0, v2, v101
	v_mul_f32_e32 v2, 0x3a000000, v8
	v_cvt_pk_bf16_f32 v2, v2, v2
	s_nop 0
	v_bfi_b32 v170, s0, v2, v100
	v_mul_f32_e32 v2, 0x3a000000, v9
	v_cvt_pk_bf16_f32 v2, v2, v2
	s_nop 0
	v_bfi_b32 v174, s0, v2, v99
	v_mul_f32_e32 v2, 0x3a000000, v10
	v_cvt_pk_bf16_f32 v2, v2, v2
	s_nop 0
	v_bfi_b32 v178, s0, v2, v96
	v_mul_f32_e32 v2, 0x3a000000, v11
	v_cvt_pk_bf16_f32 v2, v2, v2
	s_nop 0
	v_bfi_b32 v182, s0, v2, v95
	v_mul_f32_e32 v2, 0x3a000000, v12
	v_cvt_pk_bf16_f32 v2, v2, v2
	s_nop 0
	v_bfi_b32 v186, s0, v2, v92
	v_mul_f32_e32 v2, 0x3a000000, v13
	v_cvt_pk_bf16_f32 v2, v2, v2
	s_nop 0
	v_bfi_b32 v190, s0, v2, v91
	v_mul_f32_e32 v2, 0x3a000000, v14
	v_cvt_pk_bf16_f32 v2, v2, v2
	s_nop 0
	v_bfi_b32 v194, s0, v2, v88
	v_mul_f32_e32 v2, 0x3a000000, v15
	v_cvt_pk_bf16_f32 v2, v2, v2
	s_nop 0
	v_bfi_b32 v198, s0, v2, v87
	v_mul_f32_e32 v2, 0x3a000000, v16
	v_cvt_pk_bf16_f32 v2, v2, v2
	s_nop 0
	v_bfi_b32 v202, s0, v2, v84
	v_mul_f32_e32 v2, 0x3a000000, v17
	v_cvt_pk_bf16_f32 v2, v2, v2
	s_nop 0
	v_bfi_b32 v206, s0, v2, v83
	ds_read_b128 v[244:247], v224
	ds_read_b128 v[250:253], v224 offset:32
	ds_read_b128 v[208:211], v224 offset:64
	s_waitcnt lgkmcnt(2)
	v_mfma_f32_32x32x16_bf16 v[2:17], v[74:77], v[244:247], 0
	ds_read_b128 v[244:247], v224 offset:96
	s_waitcnt lgkmcnt(2)
	v_mfma_f32_32x32x16_bf16 v[2:17], v[18:21], v[250:253], v[2:17]
	ds_read_b128 v[250:253], v224 offset:128
	s_waitcnt lgkmcnt(2)
	v_mfma_f32_32x32x16_bf16 v[2:17], v[22:25], v[208:211], v[2:17]
	ds_read_b128 v[208:211], v224 offset:160
	s_waitcnt lgkmcnt(2)
	v_mfma_f32_32x32x16_bf16 v[2:17], v[26:29], v[244:247], v[2:17]
	ds_read_b128 v[244:247], v224 offset:192
	s_waitcnt lgkmcnt(2)
	v_mfma_f32_32x32x16_bf16 v[2:17], v[30:33], v[250:253], v[2:17]
	ds_read_b128 v[250:253], v224 offset:224
	s_waitcnt lgkmcnt(2)
	v_mfma_f32_32x32x16_bf16 v[2:17], v[34:37], v[208:211], v[2:17]
	ds_read_b128 v[208:211], v97
	s_waitcnt lgkmcnt(2)
	v_mfma_f32_32x32x16_bf16 v[2:17], v[38:41], v[244:247], v[2:17]
	ds_read_b128 v[244:247], v225 offset:32
	s_waitcnt lgkmcnt(2)
	v_mfma_f32_32x32x16_bf16 v[2:17], v[42:45], v[250:253], v[2:17]
	ds_read_b128 v[250:253], v225 offset:64
	s_waitcnt lgkmcnt(2)
	v_mfma_f32_32x32x16_bf16 v[2:17], v[46:49], v[208:211], v[2:17]
	ds_read_b128 v[208:211], v225 offset:96
	s_waitcnt lgkmcnt(2)
	v_mfma_f32_32x32x16_bf16 v[2:17], v[50:53], v[244:247], v[2:17]
	ds_read_b128 v[244:247], v225 offset:128
	s_waitcnt lgkmcnt(2)
	v_mfma_f32_32x32x16_bf16 v[2:17], v[54:57], v[250:253], v[2:17]
	ds_read_b128 v[250:253], v225 offset:160
	s_waitcnt lgkmcnt(2)
	v_mfma_f32_32x32x16_bf16 v[2:17], v[58:61], v[208:211], v[2:17]
	ds_read_b128 v[208:211], v225 offset:192
	s_waitcnt lgkmcnt(2)
	v_mfma_f32_32x32x16_bf16 v[2:17], v[62:65], v[244:247], v[2:17]
	ds_read_b128 v[244:247], v225 offset:224
	s_waitcnt lgkmcnt(2)
	v_mfma_f32_32x32x16_bf16 v[2:17], v[66:69], v[250:253], v[2:17]
	s_waitcnt lgkmcnt(1)
	v_mfma_f32_32x32x16_bf16 v[2:17], v[70:73], v[208:211], v[2:17]
	s_waitcnt lgkmcnt(0)
	v_mfma_f32_32x32x16_bf16 v[2:17], v[78:81], v[244:247], v[2:17]
	s_nop 11
	v_mul_f32_e32 v2, 0x3a000000, v2
	v_cvt_pk_bf16_f32 v129, v2, v2
	v_mul_f32_e32 v2, 0x3a000000, v3
	v_cvt_pk_bf16_f32 v128, v2, v2
	v_mul_f32_e32 v2, 0x3a000000, v4
	v_cvt_pk_bf16_f32 v127, v2, v2
	v_mul_f32_e32 v2, 0x3a000000, v5
	v_cvt_pk_bf16_f32 v125, v2, v2
	v_mul_f32_e32 v2, 0x3a000000, v6
	v_cvt_pk_bf16_f32 v115, v2, v2
	v_mul_f32_e32 v2, 0x3a000000, v7
	v_cvt_pk_bf16_f32 v119, v2, v2
	v_mul_f32_e32 v2, 0x3a000000, v8
	v_cvt_pk_bf16_f32 v123, v2, v2
	v_mul_f32_e32 v2, 0x3a000000, v9
	v_cvt_pk_bf16_f32 v124, v2, v2
	v_mul_f32_e32 v2, 0x3a000000, v10
	v_cvt_pk_bf16_f32 v83, v2, v2
	v_mul_f32_e32 v2, 0x3a000000, v11
	v_cvt_pk_bf16_f32 v87, v2, v2
	v_mul_f32_e32 v2, 0x3a000000, v12
	v_cvt_pk_bf16_f32 v91, v2, v2
	v_mul_f32_e32 v2, 0x3a000000, v13
	v_cvt_pk_bf16_f32 v95, v2, v2
	v_mul_f32_e32 v2, 0x3a000000, v14
	v_cvt_pk_bf16_f32 v99, v2, v2
	v_mul_f32_e32 v2, 0x3a000000, v15
	v_cvt_pk_bf16_f32 v103, v2, v2
	v_mul_f32_e32 v2, 0x3a000000, v16
	v_cvt_pk_bf16_f32 v107, v2, v2
	v_mul_f32_e32 v2, 0x3a000000, v17
	v_cvt_pk_bf16_f32 v111, v2, v2
	ds_read_b128 v[244:247], v93
	ds_read_b128 v[250:253], v226 offset:32
	ds_read_b128 v[208:211], v226 offset:64
	s_waitcnt lgkmcnt(2)
	v_mfma_f32_32x32x16_bf16 v[2:17], v[74:77], v[244:247], 0
	ds_read_b128 v[244:247], v226 offset:96
	s_waitcnt lgkmcnt(2)
	v_mfma_f32_32x32x16_bf16 v[2:17], v[18:21], v[250:253], v[2:17]
	ds_read_b128 v[250:253], v226 offset:128
	s_waitcnt lgkmcnt(2)
	v_mfma_f32_32x32x16_bf16 v[2:17], v[22:25], v[208:211], v[2:17]
	ds_read_b128 v[208:211], v226 offset:160
	s_waitcnt lgkmcnt(2)
	v_mfma_f32_32x32x16_bf16 v[2:17], v[26:29], v[244:247], v[2:17]
	ds_read_b128 v[244:247], v226 offset:192
	s_waitcnt lgkmcnt(2)
	v_mfma_f32_32x32x16_bf16 v[2:17], v[30:33], v[250:253], v[2:17]
	ds_read_b128 v[250:253], v226 offset:224
	s_waitcnt lgkmcnt(2)
	v_mfma_f32_32x32x16_bf16 v[2:17], v[34:37], v[208:211], v[2:17]
	ds_read_b128 v[208:211], v89
	s_waitcnt lgkmcnt(2)
	v_mfma_f32_32x32x16_bf16 v[2:17], v[38:41], v[244:247], v[2:17]
	ds_read_b128 v[244:247], v227 offset:32
	s_waitcnt lgkmcnt(2)
	v_mfma_f32_32x32x16_bf16 v[2:17], v[42:45], v[250:253], v[2:17]
	ds_read_b128 v[250:253], v227 offset:64
	s_waitcnt lgkmcnt(2)
	v_mfma_f32_32x32x16_bf16 v[2:17], v[46:49], v[208:211], v[2:17]
	ds_read_b128 v[208:211], v227 offset:96
	s_waitcnt lgkmcnt(2)
	v_mfma_f32_32x32x16_bf16 v[2:17], v[50:53], v[244:247], v[2:17]
	ds_read_b128 v[244:247], v227 offset:128
	s_waitcnt lgkmcnt(2)
	v_mfma_f32_32x32x16_bf16 v[2:17], v[54:57], v[250:253], v[2:17]
	ds_read_b128 v[250:253], v227 offset:160
	s_waitcnt lgkmcnt(2)
	v_mfma_f32_32x32x16_bf16 v[2:17], v[58:61], v[208:211], v[2:17]
	ds_read_b128 v[208:211], v227 offset:192
	s_waitcnt lgkmcnt(2)
	v_mfma_f32_32x32x16_bf16 v[2:17], v[62:65], v[244:247], v[2:17]
	ds_read_b128 v[244:247], v227 offset:224
	s_waitcnt lgkmcnt(2)
	v_mfma_f32_32x32x16_bf16 v[2:17], v[66:69], v[250:253], v[2:17]
	s_waitcnt lgkmcnt(1)
	v_mfma_f32_32x32x16_bf16 v[2:17], v[70:73], v[208:211], v[2:17]
	s_waitcnt lgkmcnt(0)
	s_barrier
; __device__ __forceinline__ unsigned cvt2_bf16(float lo, float hi) { unsigned r; asm("v_cvt_pk_bf16_f32 %0, %1, %2" : "=v"(r) : "v"(lo), "v"(hi)); return r; }
; __device__ __forceinline__ int crow(int r, int hi) { return (r & 3) + 8 * (r >> 2) + 4 * hi; }
; __device__ __forceinline__ int crow(int r, int hi) { return (r & 3) + 8 * (r >> 2) + 4 * hi; }
; __device__ __forceinline__ int crow(int r, int hi) { return (r & 3) + 8 * (r >> 2) + 4 * hi; }
;     __device__ __forceinline__ const float* c() const { return (const float*)ld(1); }
;     __device__ __forceinline__ float* out() const { return (float*)ld(25); }
; __device__ __forceinline__ void fft_phase_split(const bf16_t* __restrict__ WCT, bf16_t* __restrict__ FB, const bf16_t* __restrict__ A1T, const bf16_t* __restrict__ A2T, const float* __restrict__ TW, char* lds, int G) {
;     ...
;       for (int c = 0; c < 8; ++c) {
;           const bf16_t* Zs = (const bf16_t*)(lds + ((c & 1) ? R_Z1 : R_Z0));
; #pragma unroll
;           for (int nbp = 0; nbp < 2; ++nbp) { const int k1o = 32 * nbp + r32; f32x16 out = f32x16{};
; #pragma unroll
;             for (int ks = 0; ks < 16; ++ks) { const bf16x8 bfr = *(const bf16x8*)(Zs + ((ks >> 3) * 64 + k1o) * ZST + (ks & 7) * 16 + 8 * hi);
;               out = __builtin_amdgcn_mfma_f32_32x32x16_bf16(a2[ks], bfr, out, 0, 0, 0); }
; #pragma unroll
;             for (int r = 0; r < 16; ++r) { const unsigned w = cvt2_bf16(out[r] * SC, out[r] * SC);
;               if ((c & 1) == 0) o[nbp][r][c >> 1] = w & 0xffffu; else o[nbp][r][c >> 1] |= w & 0xffff0000u; } }
;           if (c == 7) {
; #pragma unroll
;             for (int nbp = 0; nbp < 2; ++nbp)
; #pragma unroll
;               for (int r = 0; r < 16; ++r) { const int k = 32 * nbp + r32 + 64 * (32 * mb + crow(r, hi)); *(u32x4*)(fb + (size_t)k * 8) = o[nbp][r]; } }
;           __syncthreads();
	v_mfma_f32_32x32x16_bf16 v[2:17], v[78:81], v[244:247], v[2:17]
	s_nop 11
	v_mul_f32_e32 v2, 0x3a000000, v2
	v_cvt_pk_bf16_f32 v121, v2, v2
	v_mul_f32_e32 v2, 0x3a000000, v3
	v_cvt_pk_bf16_f32 v120, v2, v2
	v_mul_f32_e32 v2, 0x3a000000, v4
	v_cvt_pk_bf16_f32 v117, v2, v2
	v_mul_f32_e32 v2, 0x3a000000, v5
	v_cvt_pk_bf16_f32 v116, v2, v2
	v_mul_f32_e32 v2, 0x3a000000, v6
	v_cvt_pk_bf16_f32 v113, v2, v2
	v_mul_f32_e32 v2, 0x3a000000, v7
	v_cvt_pk_bf16_f32 v112, v2, v2
	v_mul_f32_e32 v2, 0x3a000000, v8
	v_cvt_pk_bf16_f32 v109, v2, v2
	v_mul_f32_e32 v2, 0x3a000000, v9
	v_cvt_pk_bf16_f32 v108, v2, v2
	v_mul_f32_e32 v2, 0x3a000000, v10
	v_cvt_pk_bf16_f32 v105, v2, v2
	v_mul_f32_e32 v2, 0x3a000000, v11
	v_cvt_pk_bf16_f32 v104, v2, v2
	v_mul_f32_e32 v2, 0x3a000000, v12
	v_cvt_pk_bf16_f32 v101, v2, v2
	v_mul_f32_e32 v2, 0x3a000000, v13
	v_cvt_pk_bf16_f32 v100, v2, v2
	v_mul_f32_e32 v2, 0x3a000000, v14
	v_cvt_pk_bf16_f32 v96, v2, v2
	v_mul_f32_e32 v2, 0x3a000000, v15
	v_cvt_pk_bf16_f32 v92, v2, v2
	v_mul_f32_e32 v2, 0x3a000000, v16
	v_cvt_pk_bf16_f32 v88, v2, v2
	v_mul_f32_e32 v2, 0x3a000000, v17
	v_cvt_pk_bf16_f32 v84, v2, v2
	ds_read_b128 v[244:247], v228
	ds_read_b128 v[250:253], v228 offset:32
	ds_read_b128 v[208:211], v228 offset:64
	s_waitcnt lgkmcnt(2)
	v_mfma_f32_32x32x16_bf16 v[2:17], v[74:77], v[244:247], 0
	ds_read_b128 v[244:247], v228 offset:96
	s_waitcnt lgkmcnt(2)
	v_mfma_f32_32x32x16_bf16 v[2:17], v[18:21], v[250:253], v[2:17]
	ds_read_b128 v[250:253], v228 offset:128
	s_waitcnt lgkmcnt(2)
	v_mfma_f32_32x32x16_bf16 v[2:17], v[22:25], v[208:211], v[2:17]
	ds_read_b128 v[208:211], v228 offset:160
	s_waitcnt lgkmcnt(2)
	v_mfma_f32_32x32x16_bf16 v[2:17], v[26:29], v[244:247], v[2:17]
	ds_read_b128 v[244:247], v228 offset:192
	s_waitcnt lgkmcnt(2)
	v_mfma_f32_32x32x16_bf16 v[2:17], v[30:33], v[250:253], v[2:17]
	ds_read_b128 v[250:253], v228 offset:224
	s_waitcnt lgkmcnt(2)
	v_mfma_f32_32x32x16_bf16 v[2:17], v[34:37], v[208:211], v[2:17]
	ds_read_b128 v[208:211], v85
	s_waitcnt lgkmcnt(2)
	v_mfma_f32_32x32x16_bf16 v[2:17], v[38:41], v[244:247], v[2:17]
	ds_read_b128 v[244:247], v229 offset:32
	s_waitcnt lgkmcnt(2)
	v_mfma_f32_32x32x16_bf16 v[2:17], v[42:45], v[250:253], v[2:17]
	ds_read_b128 v[250:253], v229 offset:64
	s_waitcnt lgkmcnt(2)
	v_mfma_f32_32x32x16_bf16 v[2:17], v[46:49], v[208:211], v[2:17]
	ds_read_b128 v[208:211], v229 offset:96
	s_waitcnt lgkmcnt(2)
	v_mfma_f32_32x32x16_bf16 v[2:17], v[50:53], v[244:247], v[2:17]
	ds_read_b128 v[244:247], v229 offset:128
	s_waitcnt lgkmcnt(2)
	v_mfma_f32_32x32x16_bf16 v[2:17], v[54:57], v[250:253], v[2:17]
	ds_read_b128 v[250:253], v229 offset:160
	s_waitcnt lgkmcnt(2)
	v_mfma_f32_32x32x16_bf16 v[2:17], v[58:61], v[208:211], v[2:17]
	ds_read_b128 v[208:211], v229 offset:192
	s_waitcnt lgkmcnt(2)
	v_mfma_f32_32x32x16_bf16 v[2:17], v[62:65], v[244:247], v[2:17]
	ds_read_b128 v[244:247], v229 offset:224
	s_waitcnt lgkmcnt(2)
	v_mfma_f32_32x32x16_bf16 v[2:17], v[66:69], v[250:253], v[2:17]
	s_waitcnt lgkmcnt(1)
	v_mfma_f32_32x32x16_bf16 v[2:17], v[70:73], v[208:211], v[2:17]
	s_waitcnt lgkmcnt(0)
	v_mfma_f32_32x32x16_bf16 v[2:17], v[78:81], v[244:247], v[2:17]
	s_nop 11
	v_mul_f32_e32 v2, 0x3a000000, v2
	v_cvt_pk_bf16_f32 v2, v2, v2
	s_nop 0
	v_bfi_b32 v131, s0, v2, v129
	v_mul_f32_e32 v2, 0x3a000000, v3
	v_cvt_pk_bf16_f32 v2, v2, v2
	s_nop 0
	v_bfi_b32 v135, s0, v2, v128
	v_mul_f32_e32 v2, 0x3a000000, v4
	v_cvt_pk_bf16_f32 v2, v2, v2
	s_nop 0
	v_bfi_b32 v139, s0, v2, v127
	v_mul_f32_e32 v2, 0x3a000000, v5
	v_cvt_pk_bf16_f32 v2, v2, v2
	s_nop 0
	v_bfi_b32 v143, s0, v2, v125
	v_mul_f32_e32 v2, 0x3a000000, v6
	v_cvt_pk_bf16_f32 v2, v2, v2
	s_nop 0
	v_bfi_b32 v115, s0, v2, v115
	v_mul_f32_e32 v2, 0x3a000000, v7
	v_cvt_pk_bf16_f32 v2, v2, v2
	s_nop 0
	v_bfi_b32 v119, s0, v2, v119
	v_mul_f32_e32 v2, 0x3a000000, v8
	v_cvt_pk_bf16_f32 v2, v2, v2
	s_nop 0
	v_bfi_b32 v123, s0, v2, v123
	v_mul_f32_e32 v2, 0x3a000000, v9
	v_cvt_pk_bf16_f32 v2, v2, v2
	s_nop 0
	v_bfi_b32 v127, s0, v2, v124
	v_mul_f32_e32 v2, 0x3a000000, v10
	v_cvt_pk_bf16_f32 v2, v2, v2
	s_nop 0
	v_bfi_b32 v83, s0, v2, v83
	v_mul_f32_e32 v2, 0x3a000000, v11
	v_cvt_pk_bf16_f32 v2, v2, v2
	s_nop 0
	v_bfi_b32 v87, s0, v2, v87
	v_mul_f32_e32 v2, 0x3a000000, v12
	v_cvt_pk_bf16_f32 v2, v2, v2
	s_nop 0
	v_bfi_b32 v91, s0, v2, v91
	v_mul_f32_e32 v2, 0x3a000000, v13
	v_cvt_pk_bf16_f32 v2, v2, v2
	s_nop 0
	v_bfi_b32 v95, s0, v2, v95
	v_mul_f32_e32 v2, 0x3a000000, v14
	v_cvt_pk_bf16_f32 v2, v2, v2
	s_nop 0
	v_bfi_b32 v99, s0, v2, v99
	v_mul_f32_e32 v2, 0x3a000000, v15
	v_cvt_pk_bf16_f32 v2, v2, v2
	s_nop 0
	v_bfi_b32 v103, s0, v2, v103
	v_mul_f32_e32 v2, 0x3a000000, v16
	v_cvt_pk_bf16_f32 v2, v2, v2
	s_nop 0
	v_bfi_b32 v107, s0, v2, v107
	v_mul_f32_e32 v2, 0x3a000000, v17
	v_cvt_pk_bf16_f32 v2, v2, v2
	s_nop 0
	v_bfi_b32 v111, s0, v2, v111
	ds_read_b128 v[244:247], v153
	ds_read_b128 v[250:253], v230 offset:32
	ds_read_b128 v[208:211], v230 offset:64
	s_waitcnt lgkmcnt(2)
	v_mfma_f32_32x32x16_bf16 v[2:17], v[74:77], v[244:247], 0
	ds_read_b128 v[244:247], v230 offset:96
	s_waitcnt lgkmcnt(2)
	v_mfma_f32_32x32x16_bf16 v[2:17], v[18:21], v[250:253], v[2:17]
	ds_read_b128 v[250:253], v230 offset:128
	s_waitcnt lgkmcnt(2)
	v_mfma_f32_32x32x16_bf16 v[2:17], v[22:25], v[208:211], v[2:17]
	ds_read_b128 v[208:211], v230 offset:160
	s_waitcnt lgkmcnt(2)
	v_mfma_f32_32x32x16_bf16 v[2:17], v[26:29], v[244:247], v[2:17]
	ds_read_b128 v[244:247], v230 offset:192
	s_waitcnt lgkmcnt(2)
	v_mfma_f32_32x32x16_bf16 v[2:17], v[30:33], v[250:253], v[2:17]
	ds_read_b128 v[250:253], v230 offset:224
	s_waitcnt lgkmcnt(2)
	v_mfma_f32_32x32x16_bf16 v[2:17], v[34:37], v[208:211], v[2:17]
	ds_read_b128 v[208:211], v149
	s_waitcnt lgkmcnt(2)
	v_mfma_f32_32x32x16_bf16 v[2:17], v[38:41], v[244:247], v[2:17]
	ds_read_b128 v[244:247], v231 offset:32
	s_waitcnt lgkmcnt(2)
	v_mfma_f32_32x32x16_bf16 v[2:17], v[42:45], v[250:253], v[2:17]
	ds_read_b128 v[250:253], v231 offset:64
	s_waitcnt lgkmcnt(2)
	v_mfma_f32_32x32x16_bf16 v[2:17], v[46:49], v[208:211], v[2:17]
	ds_read_b128 v[208:211], v231 offset:96
	s_waitcnt lgkmcnt(2)
	v_mfma_f32_32x32x16_bf16 v[2:17], v[50:53], v[244:247], v[2:17]
	ds_read_b128 v[244:247], v231 offset:128
	s_waitcnt lgkmcnt(2)
	v_mfma_f32_32x32x16_bf16 v[2:17], v[54:57], v[250:253], v[2:17]
	ds_read_b128 v[250:253], v231 offset:160
	s_waitcnt lgkmcnt(2)
	v_mfma_f32_32x32x16_bf16 v[2:17], v[58:61], v[208:211], v[2:17]
	ds_read_b128 v[208:211], v231 offset:192
	s_waitcnt lgkmcnt(2)
	v_mfma_f32_32x32x16_bf16 v[2:17], v[62:65], v[244:247], v[2:17]
	ds_read_b128 v[244:247], v231 offset:224
	s_waitcnt lgkmcnt(2)
	v_mfma_f32_32x32x16_bf16 v[2:17], v[66:69], v[250:253], v[2:17]
	s_waitcnt lgkmcnt(1)
	v_mfma_f32_32x32x16_bf16 v[2:17], v[70:73], v[208:211], v[2:17]
	s_waitcnt lgkmcnt(0)
	s_barrier
; __device__ __forceinline__ unsigned cvt2_bf16(float lo, float hi) { unsigned r; asm("v_cvt_pk_bf16_f32 %0, %1, %2" : "=v"(r) : "v"(lo), "v"(hi)); return r; }
; __device__ __forceinline__ int crow(int r, int hi) { return (r & 3) + 8 * (r >> 2) + 4 * hi; }
; __device__ __forceinline__ int crow(int r, int hi) { return (r & 3) + 8 * (r >> 2) + 4 * hi; }
; __device__ __forceinline__ int crow(int r, int hi) { return (r & 3) + 8 * (r >> 2) + 4 * hi; }
;     __device__ __forceinline__ const float* c() const { return (const float*)ld(1); }
;     __device__ __forceinline__ float* out() const { return (float*)ld(25); }
; __device__ __forceinline__ void fft_phase_split(const bf16_t* __restrict__ WCT, bf16_t* __restrict__ FB, const bf16_t* __restrict__ A1T, const bf16_t* __restrict__ A2T, const float* __restrict__ TW, char* lds, int G) {
;     ...
;       for (int c = 0; c < 8; ++c) {
;           const bf16_t* Zs = (const bf16_t*)(lds + ((c & 1) ? R_Z1 : R_Z0));
; #pragma unroll
;           for (int nbp = 0; nbp < 2; ++nbp) { const int k1o = 32 * nbp + r32; f32x16 out = f32x16{};
; #pragma unroll
;             for (int ks = 0; ks < 16; ++ks) { const bf16x8 bfr = *(const bf16x8*)(Zs + ((ks >> 3) * 64 + k1o) * ZST + (ks & 7) * 16 + 8 * hi);
;               out = __builtin_amdgcn_mfma_f32_32x32x16_bf16(a2[ks], bfr, out, 0, 0, 0); }
; #pragma unroll
;             for (int r = 0; r < 16; ++r) { const unsigned w = cvt2_bf16(out[r] * SC, out[r] * SC);
;               if ((c & 1) == 0) o[nbp][r][c >> 1] = w & 0xffffu; else o[nbp][r][c >> 1] |= w & 0xffff0000u; } }
;           if (c == 7) {
; #pragma unroll
;             for (int nbp = 0; nbp < 2; ++nbp)
; #pragma unroll
;               for (int r = 0; r < 16; ++r) { const int k = 32 * nbp + r32 + 64 * (32 * mb + crow(r, hi)); *(u32x4*)(fb + (size_t)k * 8) = o[nbp][r]; } }
;           __syncthreads();
	v_mfma_f32_32x32x16_bf16 v[2:17], v[78:81], v[244:247], v[2:17]
	s_nop 11
	v_mul_f32_e32 v2, 0x3a000000, v2
	v_cvt_pk_bf16_f32 v2, v2, v2
	s_nop 0
	v_bfi_b32 v147, s0, v2, v121
	v_mul_f32_e32 v2, 0x3a000000, v3
	v_cvt_pk_bf16_f32 v2, v2, v2
	s_nop 0
	v_bfi_b32 v151, s0, v2, v120
	v_mul_f32_e32 v2, 0x3a000000, v4
	v_cvt_pk_bf16_f32 v2, v2, v2
	s_nop 0
	v_bfi_b32 v155, s0, v2, v117
	v_mul_f32_e32 v2, 0x3a000000, v5
	v_cvt_pk_bf16_f32 v2, v2, v2
	s_nop 0
	v_bfi_b32 v159, s0, v2, v116
	v_mul_f32_e32 v2, 0x3a000000, v6
	v_cvt_pk_bf16_f32 v2, v2, v2
	s_nop 0
	v_bfi_b32 v163, s0, v2, v113
	v_mul_f32_e32 v2, 0x3a000000, v7
	v_cvt_pk_bf16_f32 v2, v2, v2
	s_nop 0
	v_bfi_b32 v167, s0, v2, v112
	v_mul_f32_e32 v2, 0x3a000000, v8
	v_cvt_pk_bf16_f32 v2, v2, v2
	s_nop 0
	v_bfi_b32 v171, s0, v2, v109
	v_mul_f32_e32 v2, 0x3a000000, v9
	v_cvt_pk_bf16_f32 v2, v2, v2
	s_nop 0
	v_bfi_b32 v175, s0, v2, v108
	v_mul_f32_e32 v2, 0x3a000000, v10
	v_cvt_pk_bf16_f32 v2, v2, v2
	s_nop 0
	v_bfi_b32 v179, s0, v2, v105
	v_mul_f32_e32 v2, 0x3a000000, v11
	v_cvt_pk_bf16_f32 v2, v2, v2
	s_nop 0
	v_bfi_b32 v183, s0, v2, v104
	v_mul_f32_e32 v2, 0x3a000000, v12
	v_cvt_pk_bf16_f32 v2, v2, v2
	s_nop 0
	v_bfi_b32 v187, s0, v2, v101
	v_mul_f32_e32 v2, 0x3a000000, v13
	v_cvt_pk_bf16_f32 v2, v2, v2
	s_nop 0
	v_bfi_b32 v191, s0, v2, v100
	v_mul_f32_e32 v2, 0x3a000000, v14
	v_cvt_pk_bf16_f32 v2, v2, v2
	s_nop 0
	v_bfi_b32 v195, s0, v2, v96
	v_mul_f32_e32 v2, 0x3a000000, v15
	v_cvt_pk_bf16_f32 v2, v2, v2
	s_nop 0
	v_bfi_b32 v199, s0, v2, v92
	v_mul_f32_e32 v2, 0x3a000000, v16
	v_cvt_pk_bf16_f32 v2, v2, v2
	s_nop 0
	v_bfi_b32 v203, s0, v2, v88
	v_mul_f32_e32 v2, 0x3a000000, v17
	v_cvt_pk_bf16_f32 v2, v2, v2
	s_nop 0
	v_bfi_b32 v207, s0, v2, v84
	ds_read_b128 v[244:247], v224
	ds_read_b128 v[250:253], v224 offset:32
	ds_read_b128 v[208:211], v224 offset:64
	s_waitcnt lgkmcnt(2)
	v_mfma_f32_32x32x16_bf16 v[2:17], v[74:77], v[244:247], 0
	ds_read_b128 v[244:247], v224 offset:96
	s_waitcnt lgkmcnt(2)
	v_mfma_f32_32x32x16_bf16 v[2:17], v[18:21], v[250:253], v[2:17]
	ds_read_b128 v[250:253], v224 offset:128
	s_waitcnt lgkmcnt(2)
	v_mfma_f32_32x32x16_bf16 v[2:17], v[22:25], v[208:211], v[2:17]
	ds_read_b128 v[208:211], v224 offset:160
	s_waitcnt lgkmcnt(2)
	v_mfma_f32_32x32x16_bf16 v[2:17], v[26:29], v[244:247], v[2:17]
	ds_read_b128 v[244:247], v224 offset:192
	s_waitcnt lgkmcnt(2)
	v_mfma_f32_32x32x16_bf16 v[2:17], v[30:33], v[250:253], v[2:17]
	ds_read_b128 v[250:253], v224 offset:224
	s_waitcnt lgkmcnt(2)
	v_mfma_f32_32x32x16_bf16 v[2:17], v[34:37], v[208:211], v[2:17]
	ds_read_b128 v[208:211], v97
	s_waitcnt lgkmcnt(2)
	v_mfma_f32_32x32x16_bf16 v[2:17], v[38:41], v[244:247], v[2:17]
	ds_read_b128 v[244:247], v225 offset:32
	s_waitcnt lgkmcnt(2)
	v_mfma_f32_32x32x16_bf16 v[2:17], v[42:45], v[250:253], v[2:17]
	ds_read_b128 v[250:253], v225 offset:64
	s_waitcnt lgkmcnt(2)
	v_mfma_f32_32x32x16_bf16 v[2:17], v[46:49], v[208:211], v[2:17]
	ds_read_b128 v[208:211], v225 offset:96
	s_waitcnt lgkmcnt(2)
	v_mfma_f32_32x32x16_bf16 v[2:17], v[50:53], v[244:247], v[2:17]
	ds_read_b128 v[244:247], v225 offset:128
	s_waitcnt lgkmcnt(2)
	v_mfma_f32_32x32x16_bf16 v[2:17], v[54:57], v[250:253], v[2:17]
	ds_read_b128 v[250:253], v225 offset:160
	s_waitcnt lgkmcnt(2)
	v_mfma_f32_32x32x16_bf16 v[2:17], v[58:61], v[208:211], v[2:17]
	ds_read_b128 v[208:211], v225 offset:192
	s_waitcnt lgkmcnt(2)
	v_mfma_f32_32x32x16_bf16 v[2:17], v[62:65], v[244:247], v[2:17]
	ds_read_b128 v[244:247], v225 offset:224
	s_waitcnt lgkmcnt(2)
	v_mfma_f32_32x32x16_bf16 v[2:17], v[66:69], v[250:253], v[2:17]
	s_waitcnt lgkmcnt(1)
	v_mfma_f32_32x32x16_bf16 v[2:17], v[70:73], v[208:211], v[2:17]
	s_waitcnt lgkmcnt(0)
	v_mfma_f32_32x32x16_bf16 v[2:17], v[78:81], v[244:247], v[2:17]
	s_nop 11
	v_mul_f32_e32 v2, 0x3a000000, v2
	v_cvt_pk_bf16_f32 v132, v2, v2
	v_mul_f32_e32 v2, 0x3a000000, v3
	v_cvt_pk_bf16_f32 v136, v2, v2
	v_mul_f32_e32 v2, 0x3a000000, v4
	v_cvt_pk_bf16_f32 v140, v2, v2
	v_mul_f32_e32 v2, 0x3a000000, v5
	v_cvt_pk_bf16_f32 v144, v2, v2
	v_mul_f32_e32 v2, 0x3a000000, v6
	v_cvt_pk_bf16_f32 v116, v2, v2
	v_mul_f32_e32 v2, 0x3a000000, v7
	v_cvt_pk_bf16_f32 v120, v2, v2
	v_mul_f32_e32 v2, 0x3a000000, v8
	v_cvt_pk_bf16_f32 v124, v2, v2
	v_mul_f32_e32 v2, 0x3a000000, v9
	v_cvt_pk_bf16_f32 v128, v2, v2
	v_mul_f32_e32 v2, 0x3a000000, v10
	v_cvt_pk_bf16_f32 v84, v2, v2
	v_mul_f32_e32 v2, 0x3a000000, v11
	v_cvt_pk_bf16_f32 v88, v2, v2
	v_mul_f32_e32 v2, 0x3a000000, v12
	v_cvt_pk_bf16_f32 v92, v2, v2
	v_mul_f32_e32 v2, 0x3a000000, v13
	v_cvt_pk_bf16_f32 v96, v2, v2
	v_mul_f32_e32 v2, 0x3a000000, v14
	v_cvt_pk_bf16_f32 v100, v2, v2
	v_mul_f32_e32 v2, 0x3a000000, v15
	v_cvt_pk_bf16_f32 v104, v2, v2
	v_mul_f32_e32 v2, 0x3a000000, v16
	v_cvt_pk_bf16_f32 v108, v2, v2
	v_mul_f32_e32 v2, 0x3a000000, v17
	v_cvt_pk_bf16_f32 v112, v2, v2
	ds_read_b128 v[244:247], v93
	ds_read_b128 v[250:253], v226 offset:32
	ds_read_b128 v[208:211], v226 offset:64
	s_waitcnt lgkmcnt(2)
	v_mfma_f32_32x32x16_bf16 v[2:17], v[74:77], v[244:247], 0
	ds_read_b128 v[244:247], v226 offset:96
	s_waitcnt lgkmcnt(2)
	v_mfma_f32_32x32x16_bf16 v[2:17], v[18:21], v[250:253], v[2:17]
	ds_read_b128 v[250:253], v226 offset:128
	s_waitcnt lgkmcnt(2)
	v_mfma_f32_32x32x16_bf16 v[2:17], v[22:25], v[208:211], v[2:17]
	ds_read_b128 v[208:211], v226 offset:160
	s_waitcnt lgkmcnt(2)
	v_mfma_f32_32x32x16_bf16 v[2:17], v[26:29], v[244:247], v[2:17]
	ds_read_b128 v[244:247], v226 offset:192
	s_waitcnt lgkmcnt(2)
	v_mfma_f32_32x32x16_bf16 v[2:17], v[30:33], v[250:253], v[2:17]
	ds_read_b128 v[250:253], v226 offset:224
	s_waitcnt lgkmcnt(2)
	v_mfma_f32_32x32x16_bf16 v[2:17], v[34:37], v[208:211], v[2:17]
	ds_read_b128 v[208:211], v89
	s_waitcnt lgkmcnt(2)
	v_mfma_f32_32x32x16_bf16 v[2:17], v[38:41], v[244:247], v[2:17]
	ds_read_b128 v[244:247], v227 offset:32
	s_waitcnt lgkmcnt(2)
	v_mfma_f32_32x32x16_bf16 v[2:17], v[42:45], v[250:253], v[2:17]
	ds_read_b128 v[250:253], v227 offset:64
	s_waitcnt lgkmcnt(2)
	v_mfma_f32_32x32x16_bf16 v[2:17], v[46:49], v[208:211], v[2:17]
	ds_read_b128 v[208:211], v227 offset:96
	s_waitcnt lgkmcnt(2)
	v_mfma_f32_32x32x16_bf16 v[2:17], v[50:53], v[244:247], v[2:17]
	ds_read_b128 v[244:247], v227 offset:128
	s_waitcnt lgkmcnt(2)
	v_mfma_f32_32x32x16_bf16 v[2:17], v[54:57], v[250:253], v[2:17]
	ds_read_b128 v[250:253], v227 offset:160
	s_waitcnt lgkmcnt(2)
	v_mfma_f32_32x32x16_bf16 v[2:17], v[58:61], v[208:211], v[2:17]
	ds_read_b128 v[208:211], v227 offset:192
	s_waitcnt lgkmcnt(2)
	v_mfma_f32_32x32x16_bf16 v[2:17], v[62:65], v[244:247], v[2:17]
	ds_read_b128 v[244:247], v227 offset:224
	s_waitcnt lgkmcnt(2)
	v_mfma_f32_32x32x16_bf16 v[2:17], v[66:69], v[250:253], v[2:17]
	s_waitcnt lgkmcnt(1)
	v_mfma_f32_32x32x16_bf16 v[2:17], v[70:73], v[208:211], v[2:17]
	s_waitcnt lgkmcnt(0)
	s_barrier
; __device__ __forceinline__ unsigned cvt2_bf16(float lo, float hi) { unsigned r; asm("v_cvt_pk_bf16_f32 %0, %1, %2" : "=v"(r) : "v"(lo), "v"(hi)); return r; }
; __device__ __forceinline__ int crow(int r, int hi) { return (r & 3) + 8 * (r >> 2) + 4 * hi; }
; __device__ __forceinline__ int crow(int r, int hi) { return (r & 3) + 8 * (r >> 2) + 4 * hi; }
; __device__ __forceinline__ int crow(int r, int hi) { return (r & 3) + 8 * (r >> 2) + 4 * hi; }
;     __device__ __forceinline__ const float* c() const { return (const float*)ld(1); }
;     __device__ __forceinline__ float* out() const { return (float*)ld(25); }
; __device__ __forceinline__ void fft_phase_split(const bf16_t* __restrict__ WCT, bf16_t* __restrict__ FB, const bf16_t* __restrict__ A1T, const bf16_t* __restrict__ A2T, const float* __restrict__ TW, char* lds, int G) {
;     ...
;       for (int c = 0; c < 8; ++c) {
;           const bf16_t* Zs = (const bf16_t*)(lds + ((c & 1) ? R_Z1 : R_Z0));
; #pragma unroll
;           for (int nbp = 0; nbp < 2; ++nbp) { const int k1o = 32 * nbp + r32; f32x16 out = f32x16{};
; #pragma unroll
;             for (int ks = 0; ks < 16; ++ks) { const bf16x8 bfr = *(const bf16x8*)(Zs + ((ks >> 3) * 64 + k1o) * ZST + (ks & 7) * 16 + 8 * hi);
;               out = __builtin_amdgcn_mfma_f32_32x32x16_bf16(a2[ks], bfr, out, 0, 0, 0); }
; #pragma unroll
;             for (int r = 0; r < 16; ++r) { const unsigned w = cvt2_bf16(out[r] * SC, out[r] * SC);
;               if ((c & 1) == 0) o[nbp][r][c >> 1] = w & 0xffffu; else o[nbp][r][c >> 1] |= w & 0xffff0000u; } }
;           if (c == 7) {
; #pragma unroll
;             for (int nbp = 0; nbp < 2; ++nbp)
; #pragma unroll
;               for (int r = 0; r < 16; ++r) { const int k = 32 * nbp + r32 + 64 * (32 * mb + crow(r, hi)); *(u32x4*)(fb + (size_t)k * 8) = o[nbp][r]; } }
;           __syncthreads();
	v_mfma_f32_32x32x16_bf16 v[2:17], v[78:81], v[244:247], v[2:17]
	s_nop 11
	v_mul_f32_e32 v2, 0x3a000000, v2
	v_cvt_pk_bf16_f32 v148, v2, v2
	v_mul_f32_e32 v2, 0x3a000000, v3
	v_cvt_pk_bf16_f32 v152, v2, v2
	v_mul_f32_e32 v2, 0x3a000000, v4
	v_cvt_pk_bf16_f32 v156, v2, v2
	v_mul_f32_e32 v2, 0x3a000000, v5
	v_cvt_pk_bf16_f32 v157, v2, v2
	v_mul_f32_e32 v2, 0x3a000000, v6
	v_cvt_pk_bf16_f32 v145, v2, v2
	v_mul_f32_e32 v2, 0x3a000000, v7
	v_cvt_pk_bf16_f32 v141, v2, v2
	v_mul_f32_e32 v2, 0x3a000000, v8
	v_cvt_pk_bf16_f32 v137, v2, v2
	v_mul_f32_e32 v2, 0x3a000000, v9
	v_cvt_pk_bf16_f32 v133, v2, v2
	v_mul_f32_e32 v2, 0x3a000000, v10
	v_cvt_pk_bf16_f32 v129, v2, v2
	v_mul_f32_e32 v2, 0x3a000000, v11
	v_cvt_pk_bf16_f32 v125, v2, v2
	v_mul_f32_e32 v2, 0x3a000000, v12
	v_cvt_pk_bf16_f32 v121, v2, v2
	v_mul_f32_e32 v2, 0x3a000000, v13
	v_cvt_pk_bf16_f32 v117, v2, v2
	v_mul_f32_e32 v2, 0x3a000000, v14
	v_cvt_pk_bf16_f32 v113, v2, v2
	v_mul_f32_e32 v2, 0x3a000000, v15
	v_cvt_pk_bf16_f32 v109, v2, v2
	v_mul_f32_e32 v2, 0x3a000000, v16
	v_cvt_pk_bf16_f32 v105, v2, v2
	v_mul_f32_e32 v2, 0x3a000000, v17
	v_cvt_pk_bf16_f32 v101, v2, v2
	ds_read_b128 v[244:247], v228
	ds_read_b128 v[250:253], v228 offset:32
	ds_read_b128 v[208:211], v228 offset:64
	s_waitcnt lgkmcnt(2)
	v_mfma_f32_32x32x16_bf16 v[2:17], v[74:77], v[244:247], 0
	ds_read_b128 v[244:247], v228 offset:96
	s_waitcnt lgkmcnt(2)
	v_mfma_f32_32x32x16_bf16 v[2:17], v[18:21], v[250:253], v[2:17]
	ds_read_b128 v[250:253], v228 offset:128
	s_waitcnt lgkmcnt(2)
	v_mfma_f32_32x32x16_bf16 v[2:17], v[22:25], v[208:211], v[2:17]
	ds_read_b128 v[208:211], v228 offset:160
	s_waitcnt lgkmcnt(2)
	v_mfma_f32_32x32x16_bf16 v[2:17], v[26:29], v[244:247], v[2:17]
	ds_read_b128 v[244:247], v228 offset:192
	s_waitcnt lgkmcnt(2)
	v_mfma_f32_32x32x16_bf16 v[2:17], v[30:33], v[250:253], v[2:17]
	ds_read_b128 v[250:253], v228 offset:224
	s_waitcnt lgkmcnt(2)
	v_mfma_f32_32x32x16_bf16 v[2:17], v[34:37], v[208:211], v[2:17]
	ds_read_b128 v[208:211], v85
	s_waitcnt lgkmcnt(2)
	v_mfma_f32_32x32x16_bf16 v[2:17], v[38:41], v[244:247], v[2:17]
	ds_read_b128 v[244:247], v229 offset:32
	s_waitcnt lgkmcnt(2)
	v_mfma_f32_32x32x16_bf16 v[2:17], v[42:45], v[250:253], v[2:17]
	ds_read_b128 v[250:253], v229 offset:64
	s_waitcnt lgkmcnt(2)
	v_mfma_f32_32x32x16_bf16 v[2:17], v[46:49], v[208:211], v[2:17]
	ds_read_b128 v[208:211], v229 offset:96
	s_waitcnt lgkmcnt(2)
	v_mfma_f32_32x32x16_bf16 v[2:17], v[50:53], v[244:247], v[2:17]
	ds_read_b128 v[244:247], v229 offset:128
	s_waitcnt lgkmcnt(2)
	v_mfma_f32_32x32x16_bf16 v[2:17], v[54:57], v[250:253], v[2:17]
	ds_read_b128 v[250:253], v229 offset:160
	s_waitcnt lgkmcnt(2)
	v_mfma_f32_32x32x16_bf16 v[2:17], v[58:61], v[208:211], v[2:17]
	ds_read_b128 v[208:211], v229 offset:192
	s_waitcnt lgkmcnt(2)
	v_mfma_f32_32x32x16_bf16 v[2:17], v[62:65], v[244:247], v[2:17]
	ds_read_b128 v[244:247], v229 offset:224
	s_waitcnt lgkmcnt(2)
	v_mfma_f32_32x32x16_bf16 v[2:17], v[66:69], v[250:253], v[2:17]
	s_waitcnt lgkmcnt(1)
	v_mfma_f32_32x32x16_bf16 v[2:17], v[70:73], v[208:211], v[2:17]
	s_waitcnt lgkmcnt(0)
	v_mfma_f32_32x32x16_bf16 v[2:17], v[78:81], v[244:247], v[2:17]
	s_nop 11
	v_mul_f32_e32 v2, 0x3a000000, v2
	v_cvt_pk_bf16_f32 v2, v2, v2
	s_nop 0
	v_bfi_b32 v132, s0, v2, v132
	v_mul_f32_e32 v2, 0x3a000000, v3
	v_cvt_pk_bf16_f32 v2, v2, v2
	s_nop 0
	v_bfi_b32 v136, s0, v2, v136
	v_mul_f32_e32 v2, 0x3a000000, v4
	v_cvt_pk_bf16_f32 v2, v2, v2
	s_nop 0
	v_bfi_b32 v140, s0, v2, v140
	v_mul_f32_e32 v2, 0x3a000000, v5
	v_cvt_pk_bf16_f32 v2, v2, v2
	s_nop 0
	v_bfi_b32 v144, s0, v2, v144
	v_mul_f32_e32 v2, 0x3a000000, v6
	v_cvt_pk_bf16_f32 v2, v2, v2
	s_nop 0
	v_bfi_b32 v116, s0, v2, v116
	v_mul_f32_e32 v2, 0x3a000000, v7
	v_cvt_pk_bf16_f32 v2, v2, v2
	s_nop 0
	v_bfi_b32 v120, s0, v2, v120
	v_mul_f32_e32 v2, 0x3a000000, v8
	v_cvt_pk_bf16_f32 v2, v2, v2
	s_nop 0
	v_bfi_b32 v124, s0, v2, v124
	v_mul_f32_e32 v2, 0x3a000000, v9
	v_cvt_pk_bf16_f32 v2, v2, v2
	s_nop 0
	v_bfi_b32 v128, s0, v2, v128
	v_mul_f32_e32 v2, 0x3a000000, v10
	v_cvt_pk_bf16_f32 v2, v2, v2
	s_nop 0
	v_bfi_b32 v84, s0, v2, v84
	v_mul_f32_e32 v2, 0x3a000000, v11
	v_cvt_pk_bf16_f32 v2, v2, v2
	s_nop 0
	v_bfi_b32 v88, s0, v2, v88
	v_mul_f32_e32 v2, 0x3a000000, v12
	v_cvt_pk_bf16_f32 v2, v2, v2
	s_nop 0
	v_bfi_b32 v92, s0, v2, v92
	v_mul_f32_e32 v2, 0x3a000000, v13
	v_cvt_pk_bf16_f32 v2, v2, v2
	s_nop 0
	v_bfi_b32 v96, s0, v2, v96
	v_mul_f32_e32 v2, 0x3a000000, v14
	v_cvt_pk_bf16_f32 v2, v2, v2
	s_nop 0
	v_bfi_b32 v100, s0, v2, v100
	v_mul_f32_e32 v2, 0x3a000000, v15
	v_cvt_pk_bf16_f32 v2, v2, v2
	s_nop 0
	v_bfi_b32 v104, s0, v2, v104
	v_mul_f32_e32 v2, 0x3a000000, v16
	v_cvt_pk_bf16_f32 v2, v2, v2
	s_nop 0
	v_bfi_b32 v108, s0, v2, v108
	v_mul_f32_e32 v2, 0x3a000000, v17
	v_cvt_pk_bf16_f32 v2, v2, v2
	s_nop 0
	v_bfi_b32 v112, s0, v2, v112
	ds_read_b128 v[244:247], v153
	ds_read_b128 v[250:253], v230 offset:32
	ds_read_b128 v[208:211], v230 offset:64
	s_waitcnt lgkmcnt(2)
	v_mfma_f32_32x32x16_bf16 v[2:17], v[74:77], v[244:247], 0
	ds_read_b128 v[244:247], v230 offset:96
	s_waitcnt lgkmcnt(2)
	v_mfma_f32_32x32x16_bf16 v[2:17], v[18:21], v[250:253], v[2:17]
	ds_read_b128 v[250:253], v230 offset:128
	s_waitcnt lgkmcnt(2)
	v_mfma_f32_32x32x16_bf16 v[2:17], v[22:25], v[208:211], v[2:17]
	ds_read_b128 v[208:211], v230 offset:160
	s_waitcnt lgkmcnt(2)
	v_mfma_f32_32x32x16_bf16 v[2:17], v[26:29], v[244:247], v[2:17]
	ds_read_b128 v[244:247], v230 offset:192
	s_waitcnt lgkmcnt(2)
	v_mfma_f32_32x32x16_bf16 v[2:17], v[30:33], v[250:253], v[2:17]
	ds_read_b128 v[250:253], v230 offset:224
	s_waitcnt lgkmcnt(2)
	v_mfma_f32_32x32x16_bf16 v[2:17], v[34:37], v[208:211], v[2:17]
	ds_read_b128 v[208:211], v149
	s_waitcnt lgkmcnt(2)
	v_mfma_f32_32x32x16_bf16 v[2:17], v[38:41], v[244:247], v[2:17]
	ds_read_b128 v[244:247], v231 offset:32
	s_waitcnt lgkmcnt(2)
	v_mfma_f32_32x32x16_bf16 v[2:17], v[42:45], v[250:253], v[2:17]
	ds_read_b128 v[250:253], v231 offset:64
	s_waitcnt lgkmcnt(2)
	v_mfma_f32_32x32x16_bf16 v[2:17], v[46:49], v[208:211], v[2:17]
	ds_read_b128 v[208:211], v231 offset:96
	s_waitcnt lgkmcnt(2)
	v_mfma_f32_32x32x16_bf16 v[2:17], v[50:53], v[244:247], v[2:17]
	ds_read_b128 v[244:247], v231 offset:128
	s_waitcnt lgkmcnt(2)
	v_mfma_f32_32x32x16_bf16 v[2:17], v[54:57], v[250:253], v[2:17]
	ds_read_b128 v[250:253], v231 offset:160
	s_waitcnt lgkmcnt(2)
	v_mfma_f32_32x32x16_bf16 v[2:17], v[58:61], v[208:211], v[2:17]
	ds_read_b128 v[208:211], v231 offset:192
	s_waitcnt lgkmcnt(2)
	v_mfma_f32_32x32x16_bf16 v[2:17], v[62:65], v[244:247], v[2:17]
	ds_read_b128 v[244:247], v231 offset:224
	s_waitcnt lgkmcnt(2)
	v_mfma_f32_32x32x16_bf16 v[2:17], v[66:69], v[250:253], v[2:17]
	s_waitcnt lgkmcnt(1)
	v_mfma_f32_32x32x16_bf16 v[2:17], v[70:73], v[208:211], v[2:17]
	s_waitcnt lgkmcnt(0)
	s_barrier
; __device__ __forceinline__ unsigned cvt2_bf16(float lo, float hi) { unsigned r; asm("v_cvt_pk_bf16_f32 %0, %1, %2" : "=v"(r) : "v"(lo), "v"(hi)); return r; }
;     __device__ __forceinline__ const float* c() const { return (const float*)ld(1); }
;     __device__ __forceinline__ float* out() const { return (float*)ld(25); }
; __device__ __forceinline__ void fft_phase_split(const bf16_t* __restrict__ WCT, bf16_t* __restrict__ FB, const bf16_t* __restrict__ A1T, const bf16_t* __restrict__ A2T, const float* __restrict__ TW, char* lds, int G) {
;     ...
;       for (int c = 0; c < 8; ++c) {
;           const bf16_t* Zs = (const bf16_t*)(lds + ((c & 1) ? R_Z1 : R_Z0));
; #pragma unroll
;           for (int nbp = 0; nbp < 2; ++nbp) { const int k1o = 32 * nbp + r32; f32x16 out = f32x16{};
; #pragma unroll
;             for (int ks = 0; ks < 16; ++ks) { const bf16x8 bfr = *(const bf16x8*)(Zs + ((ks >> 3) * 64 + k1o) * ZST + (ks & 7) * 16 + 8 * hi);
;               out = __builtin_amdgcn_mfma_f32_32x32x16_bf16(a2[ks], bfr, out, 0, 0, 0); }
; #pragma unroll
;             for (int r = 0; r < 16; ++r) { const unsigned w = cvt2_bf16(out[r] * SC, out[r] * SC);
;               if ((c & 1) == 0) o[nbp][r][c >> 1] = w & 0xffffu; else o[nbp][r][c >> 1] |= w & 0xffff0000u; } }
	v_mfma_f32_32x32x16_bf16 v[2:17], v[78:81], v[244:247], v[2:17]
	s_nop 11
	v_mul_f32_e32 v2, 0x3a000000, v2
	v_cvt_pk_bf16_f32 v2, v2, v2
	s_nop 0
	v_bfi_b32 v148, s0, v2, v148
	v_mul_f32_e32 v2, 0x3a000000, v3
	v_cvt_pk_bf16_f32 v2, v2, v2
	s_nop 0
	v_bfi_b32 v152, s0, v2, v152
	v_mul_f32_e32 v2, 0x3a000000, v4
	v_cvt_pk_bf16_f32 v2, v2, v2
	s_nop 0
	v_bfi_b32 v156, s0, v2, v156
	v_mul_f32_e32 v2, 0x3a000000, v5
	v_cvt_pk_bf16_f32 v2, v2, v2
	s_nop 0
	v_bfi_b32 v160, s0, v2, v157
	v_mul_f32_e32 v2, 0x3a000000, v6
	v_cvt_pk_bf16_f32 v2, v2, v2
	s_nop 0
	v_bfi_b32 v164, s0, v2, v145
	v_mul_f32_e32 v2, 0x3a000000, v7
	v_cvt_pk_bf16_f32 v2, v2, v2
	s_nop 0
	v_bfi_b32 v168, s0, v2, v141
	v_mul_f32_e32 v2, 0x3a000000, v8
	v_cvt_pk_bf16_f32 v2, v2, v2
	s_nop 0
	v_bfi_b32 v172, s0, v2, v137
	v_mul_f32_e32 v2, 0x3a000000, v9
	v_cvt_pk_bf16_f32 v2, v2, v2
	s_nop 0
	v_bfi_b32 v176, s0, v2, v133
	v_mul_f32_e32 v2, 0x3a000000, v10
	v_cvt_pk_bf16_f32 v2, v2, v2
	s_nop 0
	v_bfi_b32 v180, s0, v2, v129
	v_mul_f32_e32 v2, 0x3a000000, v11
	v_cvt_pk_bf16_f32 v2, v2, v2
	s_nop 0
	v_bfi_b32 v184, s0, v2, v125
	v_mul_f32_e32 v2, 0x3a000000, v12
	v_cvt_pk_bf16_f32 v2, v2, v2
	s_nop 0
	v_bfi_b32 v188, s0, v2, v121
	v_mul_f32_e32 v2, 0x3a000000, v13
	v_cvt_pk_bf16_f32 v2, v2, v2
	s_nop 0
	v_bfi_b32 v192, s0, v2, v117
	v_mul_f32_e32 v2, 0x3a000000, v14
	v_cvt_pk_bf16_f32 v2, v2, v2
	s_nop 0
	v_bfi_b32 v196, s0, v2, v113
	v_mul_f32_e32 v2, 0x3a000000, v15
	v_cvt_pk_bf16_f32 v2, v2, v2
	s_nop 0
	v_bfi_b32 v200, s0, v2, v109
	v_mul_f32_e32 v2, 0x3a000000, v16
	v_cvt_pk_bf16_f32 v2, v2, v2
	s_nop 0
	v_bfi_b32 v204, s0, v2, v105
	v_mul_f32_e32 v2, 0x3a000000, v17
	v_cvt_pk_bf16_f32 v2, v2, v2
	s_nop 0
	v_bfi_b32 v208, s0, v2, v101
	ds_read_b128 v[244:247], v224
	ds_read_b128 v[250:253], v224 offset:32
	ds_read_b128 v[210:213], v224 offset:64
	s_waitcnt lgkmcnt(2)
	v_mfma_f32_32x32x16_bf16 v[2:17], v[74:77], v[244:247], 0
	ds_read_b128 v[244:247], v224 offset:96
	s_waitcnt lgkmcnt(2)
	v_mfma_f32_32x32x16_bf16 v[2:17], v[18:21], v[250:253], v[2:17]
	ds_read_b128 v[250:253], v224 offset:128
	s_waitcnt lgkmcnt(2)
	v_mfma_f32_32x32x16_bf16 v[2:17], v[22:25], v[210:213], v[2:17]
	ds_read_b128 v[210:213], v224 offset:160
	s_waitcnt lgkmcnt(2)
	v_mfma_f32_32x32x16_bf16 v[2:17], v[26:29], v[244:247], v[2:17]
	ds_read_b128 v[244:247], v224 offset:192
	s_waitcnt lgkmcnt(2)
	v_mfma_f32_32x32x16_bf16 v[2:17], v[30:33], v[250:253], v[2:17]
	ds_read_b128 v[250:253], v224 offset:224
	s_waitcnt lgkmcnt(2)
	v_mfma_f32_32x32x16_bf16 v[2:17], v[34:37], v[210:213], v[2:17]
	ds_read_b128 v[210:213], v97
	s_waitcnt lgkmcnt(2)
	v_mfma_f32_32x32x16_bf16 v[2:17], v[38:41], v[244:247], v[2:17]
	ds_read_b128 v[244:247], v225 offset:32
	s_waitcnt lgkmcnt(2)
	v_mfma_f32_32x32x16_bf16 v[2:17], v[42:45], v[250:253], v[2:17]
	ds_read_b128 v[250:253], v225 offset:64
	s_waitcnt lgkmcnt(2)
	v_mfma_f32_32x32x16_bf16 v[2:17], v[46:49], v[210:213], v[2:17]
	ds_read_b128 v[210:213], v225 offset:96
	s_waitcnt lgkmcnt(2)
	v_mfma_f32_32x32x16_bf16 v[2:17], v[50:53], v[244:247], v[2:17]
	ds_read_b128 v[244:247], v225 offset:128
	s_waitcnt lgkmcnt(2)
	v_mfma_f32_32x32x16_bf16 v[2:17], v[54:57], v[250:253], v[2:17]
	ds_read_b128 v[250:253], v225 offset:160
	s_waitcnt lgkmcnt(2)
	v_mfma_f32_32x32x16_bf16 v[2:17], v[58:61], v[210:213], v[2:17]
	ds_read_b128 v[210:213], v225 offset:192
	s_waitcnt lgkmcnt(2)
	v_mfma_f32_32x32x16_bf16 v[2:17], v[62:65], v[244:247], v[2:17]
	ds_read_b128 v[244:247], v225 offset:224
	s_waitcnt lgkmcnt(2)
	v_mfma_f32_32x32x16_bf16 v[2:17], v[66:69], v[250:253], v[2:17]
	s_waitcnt lgkmcnt(1)
	v_mfma_f32_32x32x16_bf16 v[2:17], v[70:73], v[210:213], v[2:17]
	s_waitcnt lgkmcnt(0)
	v_mfma_f32_32x32x16_bf16 v[2:17], v[78:81], v[244:247], v[2:17]
	s_nop 11
	v_mul_f32_e32 v2, 0x3a000000, v2
	v_cvt_pk_bf16_f32 v133, v2, v2
	v_mul_f32_e32 v2, 0x3a000000, v3
	v_cvt_pk_bf16_f32 v137, v2, v2
	v_mul_f32_e32 v2, 0x3a000000, v4
	v_cvt_pk_bf16_f32 v141, v2, v2
	v_mul_f32_e32 v2, 0x3a000000, v5
	v_cvt_pk_bf16_f32 v145, v2, v2
	v_mul_f32_e32 v2, 0x3a000000, v6
	v_cvt_pk_bf16_f32 v117, v2, v2
	v_mul_f32_e32 v2, 0x3a000000, v7
	v_cvt_pk_bf16_f32 v121, v2, v2
	v_mul_f32_e32 v2, 0x3a000000, v8
	v_cvt_pk_bf16_f32 v125, v2, v2
	v_mul_f32_e32 v2, 0x3a000000, v9
	v_cvt_pk_bf16_f32 v129, v2, v2
	v_mul_f32_e32 v2, 0x3a000000, v10
	v_cvt_pk_bf16_f32 v212, v2, v2
	v_mul_f32_e32 v2, 0x3a000000, v11
	v_cvt_pk_bf16_f32 v211, v2, v2
	v_mul_f32_e32 v2, 0x3a000000, v12
	v_cvt_pk_bf16_f32 v210, v2, v2
	v_mul_f32_e32 v2, 0x3a000000, v13
	v_cvt_pk_bf16_f32 v97, v2, v2
	v_mul_f32_e32 v2, 0x3a000000, v14
	v_cvt_pk_bf16_f32 v101, v2, v2
	v_mul_f32_e32 v2, 0x3a000000, v15
	v_cvt_pk_bf16_f32 v105, v2, v2
	v_mul_f32_e32 v2, 0x3a000000, v16
	v_cvt_pk_bf16_f32 v109, v2, v2
	v_mul_f32_e32 v2, 0x3a000000, v17
	v_cvt_pk_bf16_f32 v113, v2, v2
	ds_read_b128 v[244:247], v93
	ds_read_b128 v[250:253], v226 offset:32
	ds_read_b128 v[232:235], v226 offset:64
	s_waitcnt lgkmcnt(2)
	v_mfma_f32_32x32x16_bf16 v[2:17], v[74:77], v[244:247], 0
	ds_read_b128 v[244:247], v226 offset:96
	s_waitcnt lgkmcnt(2)
	v_mfma_f32_32x32x16_bf16 v[2:17], v[18:21], v[250:253], v[2:17]
	ds_read_b128 v[250:253], v226 offset:128
	s_waitcnt lgkmcnt(2)
	v_mfma_f32_32x32x16_bf16 v[2:17], v[22:25], v[232:235], v[2:17]
	ds_read_b128 v[232:235], v226 offset:160
	s_waitcnt lgkmcnt(2)
	v_mfma_f32_32x32x16_bf16 v[2:17], v[26:29], v[244:247], v[2:17]
	ds_read_b128 v[244:247], v226 offset:192
	s_waitcnt lgkmcnt(2)
	v_mfma_f32_32x32x16_bf16 v[2:17], v[30:33], v[250:253], v[2:17]
	ds_read_b128 v[250:253], v226 offset:224
	s_waitcnt lgkmcnt(2)
	v_mfma_f32_32x32x16_bf16 v[2:17], v[34:37], v[232:235], v[2:17]
	ds_read_b128 v[232:235], v89
	s_waitcnt lgkmcnt(2)
	v_mfma_f32_32x32x16_bf16 v[2:17], v[38:41], v[244:247], v[2:17]
	ds_read_b128 v[244:247], v227 offset:32
	s_waitcnt lgkmcnt(2)
	v_mfma_f32_32x32x16_bf16 v[2:17], v[42:45], v[250:253], v[2:17]
	ds_read_b128 v[250:253], v227 offset:64
	s_waitcnt lgkmcnt(2)
	v_mfma_f32_32x32x16_bf16 v[2:17], v[46:49], v[232:235], v[2:17]
	ds_read_b128 v[232:235], v227 offset:96
	s_waitcnt lgkmcnt(2)
	v_mfma_f32_32x32x16_bf16 v[2:17], v[50:53], v[244:247], v[2:17]
	ds_read_b128 v[244:247], v227 offset:128
	s_waitcnt lgkmcnt(2)
	v_mfma_f32_32x32x16_bf16 v[2:17], v[54:57], v[250:253], v[2:17]
	ds_read_b128 v[250:253], v227 offset:160
	s_waitcnt lgkmcnt(2)
	v_mfma_f32_32x32x16_bf16 v[2:17], v[58:61], v[232:235], v[2:17]
	ds_read_b128 v[232:235], v227 offset:192
	s_waitcnt lgkmcnt(2)
	v_mfma_f32_32x32x16_bf16 v[2:17], v[62:65], v[244:247], v[2:17]
	ds_read_b128 v[244:247], v227 offset:224
	s_waitcnt lgkmcnt(2)
	v_mfma_f32_32x32x16_bf16 v[2:17], v[66:69], v[250:253], v[2:17]
	s_waitcnt lgkmcnt(1)
	v_mfma_f32_32x32x16_bf16 v[2:17], v[70:73], v[232:235], v[2:17]
	s_waitcnt lgkmcnt(0)
	s_barrier
; __device__ __forceinline__ unsigned cvt2_bf16(float lo, float hi) { unsigned r; asm("v_cvt_pk_bf16_f32 %0, %1, %2" : "=v"(r) : "v"(lo), "v"(hi)); return r; }
;     __device__ __forceinline__ const float* c() const { return (const float*)ld(1); }
;     __device__ __forceinline__ float* out() const { return (float*)ld(25); }
; __device__ __forceinline__ void fft_phase_split(const bf16_t* __restrict__ WCT, bf16_t* __restrict__ FB, const bf16_t* __restrict__ A1T, const bf16_t* __restrict__ A2T, const float* __restrict__ TW, char* lds, int G) {
;     ...
;       for (int c = 0; c < 8; ++c) {
;           const bf16_t* Zs = (const bf16_t*)(lds + ((c & 1) ? R_Z1 : R_Z0));
; #pragma unroll
;           for (int nbp = 0; nbp < 2; ++nbp) { const int k1o = 32 * nbp + r32; f32x16 out = f32x16{};
; #pragma unroll
;             for (int ks = 0; ks < 16; ++ks) { const bf16x8 bfr = *(const bf16x8*)(Zs + ((ks >> 3) * 64 + k1o) * ZST + (ks & 7) * 16 + 8 * hi);
;               out = __builtin_amdgcn_mfma_f32_32x32x16_bf16(a2[ks], bfr, out, 0, 0, 0); }
; #pragma unroll
;             for (int r = 0; r < 16; ++r) { const unsigned w = cvt2_bf16(out[r] * SC, out[r] * SC);
;               if ((c & 1) == 0) o[nbp][r][c >> 1] = w & 0xffffu; else o[nbp][r][c >> 1] |= w & 0xffff0000u; } }
	v_mfma_f32_32x32x16_bf16 v[2:17], v[78:81], v[244:247], v[2:17]
	s_nop 11
	v_mul_f32_e32 v2, 0x3a000000, v2
	v_cvt_pk_bf16_f32 v233, v2, v2
	v_mul_f32_e32 v2, 0x3a000000, v3
	v_cvt_pk_bf16_f32 v232, v2, v2
	v_mul_f32_e32 v2, 0x3a000000, v4
	v_cvt_pk_bf16_f32 v157, v2, v2
	v_mul_f32_e32 v2, 0x3a000000, v5
	v_cvt_pk_bf16_f32 v161, v2, v2
	v_mul_f32_e32 v2, 0x3a000000, v6
	v_cvt_pk_bf16_f32 v165, v2, v2
	v_mul_f32_e32 v2, 0x3a000000, v7
	v_cvt_pk_bf16_f32 v169, v2, v2
	v_mul_f32_e32 v2, 0x3a000000, v8
	v_cvt_pk_bf16_f32 v173, v2, v2
	v_mul_f32_e32 v2, 0x3a000000, v9
	v_cvt_pk_bf16_f32 v177, v2, v2
	v_mul_f32_e32 v2, 0x3a000000, v10
	v_cvt_pk_bf16_f32 v181, v2, v2
	v_mul_f32_e32 v2, 0x3a000000, v11
	v_cvt_pk_bf16_f32 v185, v2, v2
	v_mul_f32_e32 v2, 0x3a000000, v12
	v_cvt_pk_bf16_f32 v189, v2, v2
	v_mul_f32_e32 v2, 0x3a000000, v13
	v_cvt_pk_bf16_f32 v193, v2, v2
	v_mul_f32_e32 v2, 0x3a000000, v14
	v_cvt_pk_bf16_f32 v197, v2, v2
	v_mul_f32_e32 v2, 0x3a000000, v15
	v_cvt_pk_bf16_f32 v201, v2, v2
	v_mul_f32_e32 v2, 0x3a000000, v16
	v_cvt_pk_bf16_f32 v205, v2, v2
	v_mul_f32_e32 v2, 0x3a000000, v17
	v_cvt_pk_bf16_f32 v209, v2, v2
	ds_read_b128 v[244:247], v228
	ds_read_b128 v[250:253], v228 offset:32
	ds_read_b128 v[234:237], v228 offset:64
	s_waitcnt lgkmcnt(2)
	v_mfma_f32_32x32x16_bf16 v[2:17], v[74:77], v[244:247], 0
	ds_read_b128 v[244:247], v228 offset:96
	s_waitcnt lgkmcnt(2)
	v_mfma_f32_32x32x16_bf16 v[2:17], v[18:21], v[250:253], v[2:17]
	ds_read_b128 v[250:253], v228 offset:128
	s_waitcnt lgkmcnt(2)
	v_mfma_f32_32x32x16_bf16 v[2:17], v[22:25], v[234:237], v[2:17]
	ds_read_b128 v[234:237], v228 offset:160
	s_waitcnt lgkmcnt(2)
	v_mfma_f32_32x32x16_bf16 v[2:17], v[26:29], v[244:247], v[2:17]
	ds_read_b128 v[244:247], v228 offset:192
	s_waitcnt lgkmcnt(2)
	v_mfma_f32_32x32x16_bf16 v[2:17], v[30:33], v[250:253], v[2:17]
	ds_read_b128 v[250:253], v228 offset:224
	s_waitcnt lgkmcnt(2)
	v_mfma_f32_32x32x16_bf16 v[2:17], v[34:37], v[234:237], v[2:17]
	ds_read_b128 v[234:237], v85
	s_waitcnt lgkmcnt(2)
	v_mfma_f32_32x32x16_bf16 v[2:17], v[38:41], v[244:247], v[2:17]
	ds_read_b128 v[244:247], v229 offset:32
	s_waitcnt lgkmcnt(2)
	v_mfma_f32_32x32x16_bf16 v[2:17], v[42:45], v[250:253], v[2:17]
	ds_read_b128 v[250:253], v229 offset:64
	s_waitcnt lgkmcnt(2)
	v_mfma_f32_32x32x16_bf16 v[2:17], v[46:49], v[234:237], v[2:17]
	ds_read_b128 v[234:237], v229 offset:96
	s_waitcnt lgkmcnt(2)
	v_mfma_f32_32x32x16_bf16 v[2:17], v[50:53], v[244:247], v[2:17]
	ds_read_b128 v[244:247], v229 offset:128
	s_waitcnt lgkmcnt(2)
	v_mfma_f32_32x32x16_bf16 v[2:17], v[54:57], v[250:253], v[2:17]
	ds_read_b128 v[250:253], v229 offset:160
	s_waitcnt lgkmcnt(2)
	v_mfma_f32_32x32x16_bf16 v[2:17], v[58:61], v[234:237], v[2:17]
	ds_read_b128 v[234:237], v229 offset:192
	s_waitcnt lgkmcnt(2)
	v_mfma_f32_32x32x16_bf16 v[2:17], v[62:65], v[244:247], v[2:17]
	ds_read_b128 v[244:247], v229 offset:224
	s_waitcnt lgkmcnt(2)
	v_mfma_f32_32x32x16_bf16 v[2:17], v[66:69], v[250:253], v[2:17]
	s_waitcnt lgkmcnt(1)
	v_mfma_f32_32x32x16_bf16 v[2:17], v[70:73], v[234:237], v[2:17]
	s_waitcnt lgkmcnt(0)
	v_mfma_f32_32x32x16_bf16 v[2:17], v[78:81], v[244:247], v[2:17]
	s_nop 11
	v_mul_f32_e32 v2, 0x3a000000, v2
	v_cvt_pk_bf16_f32 v2, v2, v2
	s_nop 0
	v_bfi_b32 v133, s0, v2, v133
	v_mul_f32_e32 v2, 0x3a000000, v3
	v_cvt_pk_bf16_f32 v2, v2, v2
	s_nop 0
	v_bfi_b32 v137, s0, v2, v137
	v_mul_f32_e32 v2, 0x3a000000, v4
	v_cvt_pk_bf16_f32 v2, v2, v2
	s_nop 0
	v_bfi_b32 v141, s0, v2, v141
	v_mul_f32_e32 v2, 0x3a000000, v5
	v_cvt_pk_bf16_f32 v2, v2, v2
	s_nop 0
	v_bfi_b32 v145, s0, v2, v145
	v_mul_f32_e32 v2, 0x3a000000, v6
	v_cvt_pk_bf16_f32 v2, v2, v2
	s_nop 0
	v_bfi_b32 v117, s0, v2, v117
	v_mul_f32_e32 v2, 0x3a000000, v7
	v_cvt_pk_bf16_f32 v2, v2, v2
	s_nop 0
	v_bfi_b32 v121, s0, v2, v121
	v_mul_f32_e32 v2, 0x3a000000, v8
	v_cvt_pk_bf16_f32 v2, v2, v2
	s_nop 0
	v_bfi_b32 v125, s0, v2, v125
	v_mul_f32_e32 v2, 0x3a000000, v9
	v_cvt_pk_bf16_f32 v2, v2, v2
	s_nop 0
	v_bfi_b32 v129, s0, v2, v129
	v_mul_f32_e32 v2, 0x3a000000, v10
	v_cvt_pk_bf16_f32 v2, v2, v2
	s_nop 0
	v_bfi_b32 v85, s0, v2, v212
	v_mul_f32_e32 v2, 0x3a000000, v11
	v_cvt_pk_bf16_f32 v2, v2, v2
	s_nop 0
	v_bfi_b32 v89, s0, v2, v211
	v_mul_f32_e32 v2, 0x3a000000, v12
	v_cvt_pk_bf16_f32 v2, v2, v2
	s_nop 0
	v_bfi_b32 v93, s0, v2, v210
	v_mul_f32_e32 v2, 0x3a000000, v13
	v_cvt_pk_bf16_f32 v2, v2, v2
	s_nop 0
	v_bfi_b32 v97, s0, v2, v97
	v_mul_f32_e32 v2, 0x3a000000, v14
	v_cvt_pk_bf16_f32 v2, v2, v2
	s_nop 0
	v_bfi_b32 v101, s0, v2, v101
	v_mul_f32_e32 v2, 0x3a000000, v15
	v_cvt_pk_bf16_f32 v2, v2, v2
	s_nop 0
	v_bfi_b32 v105, s0, v2, v105
	v_mul_f32_e32 v2, 0x3a000000, v16
	v_cvt_pk_bf16_f32 v2, v2, v2
	s_nop 0
	v_bfi_b32 v109, s0, v2, v109
	v_mul_f32_e32 v2, 0x3a000000, v17
	v_cvt_pk_bf16_f32 v2, v2, v2
	s_nop 0
	v_bfi_b32 v113, s0, v2, v113
	ds_read_b128 v[244:247], v153
	ds_read_b128 v[250:253], v230 offset:32
	ds_read_b128 v[210:213], v230 offset:64
	s_waitcnt lgkmcnt(2)
	v_mfma_f32_32x32x16_bf16 v[2:17], v[74:77], v[244:247], 0
	ds_read_b128 v[244:247], v230 offset:96
	s_waitcnt lgkmcnt(2)
	v_mfma_f32_32x32x16_bf16 v[2:17], v[18:21], v[250:253], v[2:17]
	ds_read_b128 v[250:253], v230 offset:128
	s_waitcnt lgkmcnt(2)
	v_mfma_f32_32x32x16_bf16 v[2:17], v[22:25], v[210:213], v[2:17]
	ds_read_b128 v[210:213], v230 offset:160
	s_waitcnt lgkmcnt(2)
; __device__ __forceinline__ unsigned cvt2_bf16(float lo, float hi) { unsigned r; asm("v_cvt_pk_bf16_f32 %0, %1, %2" : "=v"(r) : "v"(lo), "v"(hi)); return r; }
; __device__ __forceinline__ int crow(int r, int hi) { return (r & 3) + 8 * (r >> 2) + 4 * hi; }
; __device__ __forceinline__ int crow(int r, int hi) { return (r & 3) + 8 * (r >> 2) + 4 * hi; }
; __device__ __forceinline__ int crow(int r, int hi) { return (r & 3) + 8 * (r >> 2) + 4 * hi; }
;     __device__ __forceinline__ const float* c() const { return (const float*)ld(1); }
;     __device__ __forceinline__ float* out() const { return (float*)ld(25); }
; __device__ __forceinline__ void fft_phase_split(const bf16_t* __restrict__ WCT, bf16_t* __restrict__ FB, const bf16_t* __restrict__ A1T, const bf16_t* __restrict__ A2T, const float* __restrict__ TW, char* lds, int G) {
;     ...
;       for (int c = 0; c < 8; ++c) {
;           const bf16_t* Zs = (const bf16_t*)(lds + ((c & 1) ? R_Z1 : R_Z0));
; #pragma unroll
;           for (int nbp = 0; nbp < 2; ++nbp) { const int k1o = 32 * nbp + r32; f32x16 out = f32x16{};
; #pragma unroll
;             for (int ks = 0; ks < 16; ++ks) { const bf16x8 bfr = *(const bf16x8*)(Zs + ((ks >> 3) * 64 + k1o) * ZST + (ks & 7) * 16 + 8 * hi);
;               out = __builtin_amdgcn_mfma_f32_32x32x16_bf16(a2[ks], bfr, out, 0, 0, 0); }
; #pragma unroll
;             for (int r = 0; r < 16; ++r) { const unsigned w = cvt2_bf16(out[r] * SC, out[r] * SC);
;               if ((c & 1) == 0) o[nbp][r][c >> 1] = w & 0xffffu; else o[nbp][r][c >> 1] |= w & 0xffff0000u; } }
;           if (c == 7) {
; #pragma unroll
;             for (int nbp = 0; nbp < 2; ++nbp)
; #pragma unroll
;               for (int r = 0; r < 16; ++r) { const int k = 32 * nbp + r32 + 64 * (32 * mb + crow(r, hi)); *(u32x4*)(fb + (size_t)k * 8) = o[nbp][r]; } }
;           __syncthreads();
;       }
	v_mfma_f32_32x32x16_bf16 v[2:17], v[26:29], v[244:247], v[2:17]
	ds_read_b128 v[244:247], v230 offset:192
	s_waitcnt lgkmcnt(2)
	v_mfma_f32_32x32x16_bf16 v[2:17], v[30:33], v[250:253], v[2:17]
	ds_read_b128 v[250:253], v230 offset:224
	s_waitcnt lgkmcnt(2)
	v_mfma_f32_32x32x16_bf16 v[2:17], v[34:37], v[210:213], v[2:17]
	ds_read_b128 v[210:213], v149
	s_waitcnt lgkmcnt(2)
	v_mfma_f32_32x32x16_bf16 v[2:17], v[38:41], v[244:247], v[2:17]
	ds_read_b128 v[244:247], v231 offset:32
	s_waitcnt lgkmcnt(2)
	v_mfma_f32_32x32x16_bf16 v[2:17], v[42:45], v[250:253], v[2:17]
	ds_read_b128 v[250:253], v231 offset:64
	s_waitcnt lgkmcnt(2)
	v_mfma_f32_32x32x16_bf16 v[2:17], v[46:49], v[210:213], v[2:17]
	ds_read_b128 v[210:213], v231 offset:96
	s_waitcnt lgkmcnt(2)
	v_mfma_f32_32x32x16_bf16 v[2:17], v[50:53], v[244:247], v[2:17]
	ds_read_b128 v[244:247], v231 offset:128
	s_waitcnt lgkmcnt(2)
	v_mfma_f32_32x32x16_bf16 v[2:17], v[54:57], v[250:253], v[2:17]
	ds_read_b128 v[250:253], v231 offset:160
	s_waitcnt lgkmcnt(2)
	v_mfma_f32_32x32x16_bf16 v[2:17], v[58:61], v[210:213], v[2:17]
	ds_read_b128 v[210:213], v231 offset:192
	s_waitcnt lgkmcnt(2)
	v_mfma_f32_32x32x16_bf16 v[2:17], v[62:65], v[244:247], v[2:17]
	ds_read_b128 v[244:247], v231 offset:224
	s_waitcnt lgkmcnt(2)
	v_mfma_f32_32x32x16_bf16 v[2:17], v[66:69], v[250:253], v[2:17]
	s_waitcnt lgkmcnt(1)
	v_mfma_f32_32x32x16_bf16 v[2:17], v[70:73], v[210:213], v[2:17]
	s_waitcnt lgkmcnt(0)
	v_mfma_f32_32x32x16_bf16 v[2:17], v[78:81], v[244:247], v[2:17]
	s_nop 11
	v_mul_f32_e32 v2, 0x3a000000, v2
	v_cvt_pk_bf16_f32 v2, v2, v2
	s_nop 0
	v_bfi_b32 v149, s0, v2, v233
	v_mul_f32_e32 v2, 0x3a000000, v3
	v_cvt_pk_bf16_f32 v2, v2, v2
	s_nop 0
	v_bfi_b32 v153, s0, v2, v232
	v_mul_f32_e32 v2, 0x3a000000, v4
	v_cvt_pk_bf16_f32 v2, v2, v2
	s_nop 0
	v_bfi_b32 v157, s0, v2, v157
	v_mul_f32_e32 v2, 0x3a000000, v5
	v_cvt_pk_bf16_f32 v2, v2, v2
	s_nop 0
	v_bfi_b32 v161, s0, v2, v161
	v_mul_f32_e32 v2, 0x3a000000, v6
	v_cvt_pk_bf16_f32 v2, v2, v2
	s_nop 0
	v_bfi_b32 v165, s0, v2, v165
	v_mul_f32_e32 v2, 0x3a000000, v7
	v_cvt_pk_bf16_f32 v2, v2, v2
	s_nop 0
	v_bfi_b32 v169, s0, v2, v169
	v_mul_f32_e32 v2, 0x3a000000, v8
	v_cvt_pk_bf16_f32 v2, v2, v2
	s_nop 0
	v_bfi_b32 v173, s0, v2, v173
	v_mul_f32_e32 v2, 0x3a000000, v9
	v_cvt_pk_bf16_f32 v2, v2, v2
	s_nop 0
	v_bfi_b32 v177, s0, v2, v177
	v_mul_f32_e32 v2, 0x3a000000, v10
	v_cvt_pk_bf16_f32 v2, v2, v2
	s_nop 0
	v_bfi_b32 v181, s0, v2, v181
	v_mul_f32_e32 v2, 0x3a000000, v11
	v_cvt_pk_bf16_f32 v2, v2, v2
	s_nop 0
	v_bfi_b32 v185, s0, v2, v185
	v_mul_f32_e32 v2, 0x3a000000, v12
	v_cvt_pk_bf16_f32 v2, v2, v2
	s_nop 0
	v_bfi_b32 v189, s0, v2, v189
	v_mul_f32_e32 v2, 0x3a000000, v13
	v_cvt_pk_bf16_f32 v2, v2, v2
	s_nop 0
	v_bfi_b32 v193, s0, v2, v193
	v_mul_f32_e32 v2, 0x3a000000, v14
	v_cvt_pk_bf16_f32 v2, v2, v2
	s_nop 0
	v_bfi_b32 v197, s0, v2, v197
	v_mul_f32_e32 v2, 0x3a000000, v15
	v_cvt_pk_bf16_f32 v2, v2, v2
	s_nop 0
	v_bfi_b32 v201, s0, v2, v201
	v_mul_f32_e32 v2, 0x3a000000, v16
	v_cvt_pk_bf16_f32 v2, v2, v2
	s_nop 0
	v_bfi_b32 v205, s0, v2, v205
	v_mul_f32_e32 v2, 0x3a000000, v17
	v_cvt_pk_bf16_f32 v2, v2, v2
	s_nop 0
	v_bfi_b32 v209, s0, v2, v209
	v_add_co_u32_e32 v2, vcc, s1, v216
	s_nop 1
	v_addc_co_u32_e32 v3, vcc, -1, v217, vcc
	v_add_co_u32_e32 v4, vcc, s3, v216
	global_store_dwordx4 v[2:3], v[130:133], off offset:-3584
	global_store_dwordx4 v[2:3], v[134:137], off offset:-2560
	global_store_dwordx4 v[2:3], v[138:141], off offset:-1536
	global_store_dwordx4 v[2:3], v[142:145], off offset:-512
	v_addc_co_u32_e32 v5, vcc, -1, v217, vcc
	v_add_co_u32_e32 v6, vcc, s4, v216
	global_store_dwordx4 v[4:5], v[114:117], off offset:-3584
	global_store_dwordx4 v[4:5], v[118:121], off offset:-2560
	global_store_dwordx4 v[4:5], v[122:125], off offset:-1536
	global_store_dwordx4 v[4:5], v[126:129], off offset:-512
	v_addc_co_u32_e32 v7, vcc, -1, v217, vcc
	global_store_dwordx4 v[6:7], v[82:85], off offset:-3584
	global_store_dwordx4 v[6:7], v[86:89], off offset:-2560
	global_store_dwordx4 v[6:7], v[90:93], off offset:-1536
	global_store_dwordx4 v[6:7], v[94:97], off offset:-512
	global_store_dwordx4 v[216:217], v[98:101], off offset:-3584
	global_store_dwordx4 v[216:217], v[102:105], off offset:-2560
	global_store_dwordx4 v[216:217], v[106:109], off offset:-1536
	global_store_dwordx4 v[216:217], v[110:113], off offset:-512
	global_store_dwordx4 v[2:3], v[146:149], off offset:-3072
	global_store_dwordx4 v[2:3], v[150:153], off offset:-2048
	global_store_dwordx4 v[2:3], v[154:157], off offset:-1024
	global_store_dwordx4 v[2:3], v[158:161], off
	global_store_dwordx4 v[4:5], v[162:165], off offset:-3072
	global_store_dwordx4 v[4:5], v[166:169], off offset:-2048
	global_store_dwordx4 v[4:5], v[170:173], off offset:-1024
	global_store_dwordx4 v[4:5], v[174:177], off
	global_store_dwordx4 v[6:7], v[178:181], off offset:-3072
	global_store_dwordx4 v[6:7], v[182:185], off offset:-2048
	global_store_dwordx4 v[6:7], v[186:189], off offset:-1024
	global_store_dwordx4 v[6:7], v[190:193], off
	global_store_dwordx4 v[216:217], v[194:197], off offset:-3072
	global_store_dwordx4 v[216:217], v[198:201], off offset:-2048
	global_store_dwordx4 v[216:217], v[202:205], off offset:-1024
	global_store_dwordx4 v[216:217], v[206:209], off
	v_lshl_add_u64 v[216:217], v[216:217], 0, s[12:13]
	s_barrier
	s_cbranch_scc1 .LBB0_1547
